# MoE up (SwiGLU) epilogue rewritten with packed f32 math (v_pk_fma/mul/add on register pairs, two pairs interleaved, same per-element operations); + permlane/DPP for the remaining shfl_xor sums
# speedup vs baseline: 1.0399x; 1.0075x over previous
.LBB0_258:
	v_mul_f32_e32 v1, v9, v9
	v_mul_f32_e32 v7, v7, v7
	v_fmac_f32_e32 v1, v8, v8
	v_fmac_f32_e32 v7, v6, v6
	v_add_f32_e32 v1, v1, v7
	v_mul_f32_e32 v6, v25, v25
	v_mul_f32_e32 v7, v21, v21
	v_fmac_f32_e32 v6, v24, v24
	v_fmac_f32_e32 v7, v20, v20
	v_add_f32_e32 v6, v6, v7
	v_add_f32_e32 v1, v1, v6
	v_mul_f32_e32 v6, v29, v29
	v_mul_f32_e32 v7, v27, v27
	v_fmac_f32_e32 v6, v28, v28
	v_fmac_f32_e32 v7, v26, v26
	v_add_f32_e32 v6, v6, v7
	v_add_f32_e32 v1, v1, v6
	v_mul_f32_e32 v6, v33, v33
	v_mul_f32_e32 v7, v31, v31
	v_fmac_f32_e32 v6, v32, v32
	v_fmac_f32_e32 v7, v30, v30
	v_add_f32_e32 v6, v6, v7
	v_and_b32_e32 v7, 64, v222
	v_add_f32_e32 v1, v1, v6
	v_xor_b32_e32 v6, 16, v222
	v_add_u32_e32 v7, 64, v7
	v_cmp_lt_i32_e32 vcc, v6, v7
	s_lshl_b32 s28, s28, 2
	v_cmp_eq_u32_e64 s[10:11], 0, v34
	v_cndmask_b32_e32 v6, v222, v6, vcc
	v_lshlrev_b32_e32 v38, 2, v6
	s_ashr_i32 s29, s28, 31
	s_waitcnt lgkmcnt(0)
	v_mov_b32_e32 v6, v1
	s_nop 1
	v_permlane16_swap_b32_e32 v6, v1
	v_add_f32_e32 v6, v1, v6
	v_xor_b32_e32 v1, 32, v222
	v_cmp_lt_i32_e32 vcc, v1, v7
	s_nop 1
	v_cndmask_b32_e32 v1, v222, v1, vcc
	v_lshlrev_b32_e32 v39, 2, v1
	v_mov_b32_e32 v7, v6
	s_nop 1
	v_permlane32_swap_b32_e32 v7, v6
	s_and_saveexec_b64 s[34:35], s[10:11]
	s_cbranch_execz .LBB0_260
	v_lshlrev_b64 v[8:9], 6, v[4:5]
	v_lshl_add_u64 v[8:9], s[14:15], 0, v[8:9]
	v_lshl_add_u64 v[8:9], s[28:29], 2, v[8:9]
	s_lshl_b32 s2, s47, 2
	s_mov_b32 s3, s73
	v_lshl_add_u64 v[8:9], v[8:9], 0, s[2:3]
	s_waitcnt lgkmcnt(0)
	v_add_f32_e32 v1, v6, v7
	global_store_dword v[8:9], v1, off

.LBB0_276:
	v_mul_f32_e32 v1, v21, v21
	v_mul_f32_e32 v5, v11, v11
	v_fmac_f32_e32 v1, v20, v20
	v_fmac_f32_e32 v5, v10, v10
	v_add_f32_e32 v1, v1, v5
	v_mul_f32_e32 v5, v29, v29
	v_mul_f32_e32 v7, v25, v25
	v_fmac_f32_e32 v5, v28, v28
	v_fmac_f32_e32 v7, v24, v24
	v_add_f32_e32 v5, v5, v7
	v_add_f32_e32 v1, v1, v5
	v_mul_f32_e32 v5, v33, v33
	v_mul_f32_e32 v7, v31, v31
	v_fmac_f32_e32 v5, v32, v32
	v_fmac_f32_e32 v7, v30, v30
	v_add_f32_e32 v5, v5, v7
	v_add_f32_e32 v1, v1, v5
	v_mul_f32_e32 v5, v37, v37
	v_mul_f32_e32 v7, v35, v35
	v_fmac_f32_e32 v5, v36, v36
	v_fmac_f32_e32 v7, v34, v34
	v_add_f32_e32 v5, v5, v7
	v_add_f32_e32 v1, v1, v5
	s_waitcnt lgkmcnt(0)
	v_mov_b32_e32 v5, v1
	s_nop 1
	v_permlane16_swap_b32_e32 v5, v1
	v_add_f32_e32 v5, v1, v5
	v_mov_b32_e32 v7, v5
	s_nop 1
	v_permlane32_swap_b32_e32 v7, v5
	s_and_saveexec_b64 s[34:35], s[10:11]
	s_cbranch_execz .LBB0_278
	v_lshlrev_b64 v[8:9], 6, v[8:9]
	v_lshl_add_u64 v[8:9], s[14:15], 0, v[8:9]
	v_lshl_add_u64 v[8:9], s[28:29], 2, v[8:9]
	s_lshl_b32 s2, s47, 2
	s_mov_b32 s3, s73
	v_lshl_add_u64 v[8:9], v[8:9], 0, s[2:3]
	s_waitcnt lgkmcnt(0)
	v_add_f32_e32 v1, v5, v7
	global_store_dword v[8:9], v1, off

.LBB0_384:
	v_mul_f32_e32 v1, v9, v9
	v_mul_f32_e32 v2, v7, v7
	v_fmac_f32_e32 v1, v8, v8
	v_fmac_f32_e32 v2, v6, v6
	v_add_f32_e32 v1, v1, v2
	v_mul_f32_e32 v2, v25, v25
	v_mul_f32_e32 v6, v21, v21
	v_fmac_f32_e32 v2, v24, v24
	v_fmac_f32_e32 v6, v20, v20
	v_add_f32_e32 v2, v2, v6
	v_add_f32_e32 v1, v1, v2
	v_mul_f32_e32 v2, v29, v29
	v_mul_f32_e32 v6, v27, v27
	v_fmac_f32_e32 v2, v28, v28
	v_fmac_f32_e32 v6, v26, v26
	v_add_f32_e32 v2, v2, v6
	v_add_f32_e32 v1, v1, v2
	v_mul_f32_e32 v2, v13, v13
	v_mul_f32_e32 v6, v15, v15
	v_fmac_f32_e32 v2, v12, v12
	v_fmac_f32_e32 v6, v14, v14
	v_add_f32_e32 v2, v2, v6
	v_add_f32_e32 v1, v1, v2
	s_waitcnt lgkmcnt(0)
	v_mov_b32_e32 v2, v1
	s_nop 1
	v_permlane16_swap_b32_e32 v2, v1
	v_add_f32_e32 v2, v1, v2
	v_mov_b32_e32 v6, v2
	s_nop 1
	v_permlane32_swap_b32_e32 v6, v2
	s_and_saveexec_b64 s[8:9], s[10:11]
	s_cbranch_execz .LBB0_386
	v_lshlrev_b64 v[4:5], 6, v[4:5]
	v_lshl_add_u64 v[4:5], s[14:15], 0, v[4:5]
	v_lshl_add_u64 v[4:5], s[28:29], 2, v[4:5]
	s_lshl_b32 s72, s47, 2
	v_lshl_add_u64 v[4:5], v[4:5], 0, s[72:73]
	s_waitcnt lgkmcnt(0)
	v_add_f32_e32 v1, v2, v6
	global_store_dword v[4:5], v1, off

.LBB0_1125:
	s_and_b64 vcc, exec, s[0:1]
	s_cbranch_vccz .LBB0_1124
	s_cmp_lt_u32 s30, 6
	s_cselect_b64 vcc, -1, 0
	s_and_b64 s[0:1], vcc, exec
	s_cselect_b32 s0, s4, s10
	s_cselect_b32 s1, s5, s11
	s_add_u32 s0, s0, s18
	s_addc_u32 s1, s1, s19
	v_lshlrev_b32_e32 v1, 2, v31
	global_load_dwordx4 v[24:27], v1, s[0:1]
	global_load_dwordx4 v[20:23], v1, s[0:1] offset:64
	global_load_dwordx4 v[8:11], v1, s[0:1] offset:128
	global_load_dwordx4 v[4:7], v1, s[0:1] offset:192
	v_mov_b32_e32 v1, 0x3c800000
	v_mov_b32_e32 v2, 0x3b38aa3b
	v_cndmask_b32_e32 v32, v1, v2, vcc
	v_and_b32_e32 v2, 64, v222
	v_pk_mul_f32 v[28:29], v[166:167], s[74:75] op_sel_hi:[1,0]
	v_pk_mul_f32 v[36:37], v[164:165], s[74:75] op_sel_hi:[1,0]
	v_xor_b32_e32 v1, 16, v222
	v_add_u32_e32 v2, 64, v2
	v_pk_mul_f32 v[28:29], v[28:29], v[28:29]
	v_pk_mul_f32 v[36:37], v[36:37], v[36:37]
	v_cmp_lt_i32_e32 vcc, v1, v2
	v_pk_mov_b32 v[38:39], v[36:37], v[28:29] op_sel:[1,0]
	v_mov_b32_e32 v37, v29
	v_cndmask_b32_e32 v1, v222, v1, vcc
	v_pk_add_f32 v[28:29], v[38:39], v[36:37]
	v_pk_mul_f32 v[36:37], v[162:163], s[74:75] op_sel_hi:[1,0]
	v_pk_mul_f32 v[38:39], v[160:161], s[74:75] op_sel_hi:[1,0]
	v_lshlrev_b32_e32 v34, 2, v1
	v_xor_b32_e32 v1, 32, v222
	v_pk_mul_f32 v[36:37], v[36:37], v[36:37]
	v_pk_mul_f32 v[38:39], v[38:39], v[38:39]
	v_cmp_lt_i32_e32 vcc, v1, v2
	v_pk_mov_b32 v[40:41], v[38:39], v[36:37] op_sel:[1,0]
	v_mov_b32_e32 v39, v37
	v_cndmask_b32_e32 v1, v222, v1, vcc
	v_pk_add_f32 v[36:37], v[40:41], v[38:39]
	v_pk_mul_f32 v[174:175], v[152:153], s[74:75] op_sel_hi:[1,0]
	v_lshlrev_b32_e32 v33, 2, v1
	v_pk_mul_f32 v[40:41], v[156:157], s[74:75] op_sel_hi:[1,0]
	v_mul_f32_e32 v1, v174, v174
	v_mul_f32_e32 v2, v175, v175
	v_pk_add_f32 v[28:29], v[28:29], v[28:29] op_sel:[0,1] op_sel_hi:[1,0]
	v_pk_add_f32 v[36:37], v[36:37], v[36:37] op_sel:[0,1] op_sel_hi:[1,0]
	v_pk_mul_f32 v[38:39], v[158:159], s[74:75] op_sel_hi:[1,0]
	v_mov_b32_e32 v29, v1
	v_mov_b32_e32 v37, v2
	v_mul_f32_e32 v2, v41, v41
	v_pk_mul_f32 v[42:43], v[154:155], s[74:75] op_sel_hi:[1,0]
	v_pk_add_f32 v[28:29], v[28:29], v[36:37]
	v_pk_fma_f32 v[36:37], v[40:41], v[40:41], v[2:3] op_sel_hi:[1,1,0]
	v_mul_f32_e32 v2, v39, v39
	v_mul_f32_e32 v35, v42, v42
	v_mul_f32_e32 v42, v43, v43
	v_pk_fma_f32 v[38:39], v[38:39], v[38:39], v[2:3] op_sel_hi:[1,1,0]
	v_mov_b32_e32 v37, v35
	v_mov_b32_e32 v39, v42
	v_pk_add_f32 v[36:37], v[36:37], v[38:39]
	s_lshl_b32 s72, s30, 9
	v_pk_add_f32 v[28:29], v[28:29], v[36:37]
	s_mov_b32 s21, s73
	v_add_f32_e32 v1, v28, v29
	s_waitcnt lgkmcnt(0)
	v_mov_b32_e32 v2, v1
	s_nop 1
	v_permlane16_swap_b32_e32 v2, v1
	v_add_f32_e32 v1, v1, v2
	s_waitcnt lgkmcnt(0)
	v_mov_b32_e32 v2, v1
	s_nop 1
	v_permlane32_swap_b32_e32 v2, v1
	v_add_f32_e32 v1, v1, v2
	v_fmamk_f32 v1, v1, 0x3c800000, v220
	v_cmp_gt_f32_e32 vcc, s93, v1
	v_mul_f32_e32 v2, 0x4f800000, v1
	s_nop 0
	v_cndmask_b32_e32 v1, v1, v2, vcc
	v_sqrt_f32_e32 v2, v1
	s_nop 0
	v_add_u32_e32 v28, -1, v2
	v_fma_f32 v29, -v28, v2, v1
	v_cmp_ge_f32_e64 s[0:1], 0, v29
	v_add_u32_e32 v29, 1, v2
	s_nop 0
	v_cndmask_b32_e64 v28, v2, v28, s[0:1]
	v_fma_f32 v2, -v29, v2, v1
	v_cmp_lt_f32_e64 s[0:1], 0, v2
	s_nop 1
	v_cndmask_b32_e64 v2, v28, v29, s[0:1]
	v_mul_f32_e32 v28, 0x37800000, v2
	v_cndmask_b32_e32 v2, v2, v28, vcc
	v_cmp_class_f32_e32 vcc, v1, v221
	s_nop 1
	v_cndmask_b32_e32 v1, v2, v1, vcc
	v_div_scale_f32 v2, s[0:1], v1, v1, v32
	v_rcp_f32_e32 v28, v2
	s_nop 0
	v_fma_f32 v29, -v2, v28, 1.0
	v_fmac_f32_e32 v28, v29, v28
	v_div_scale_f32 v29, vcc, v32, v1, v32
	v_mul_f32_e32 v35, v29, v28
	v_fma_f32 v36, -v2, v35, v29
	v_fmac_f32_e32 v35, v36, v28
	v_fma_f32 v2, -v2, v35, v29
	v_div_fmas_f32 v2, v2, v28, v35
	v_mov_b64_e32 v[28:29], s[14:15]
	v_div_fixup_f32 v36, v2, v1, v32
	v_mad_i64_i32 v[38:39], s[0:1], v30, s96, v[28:29]
	v_lshl_add_u64 v[38:39], v[38:39], 0, s[72:73]
	v_pk_mul_f32 v[40:41], v[164:165], v[36:37] op_sel_hi:[1,0]
	v_lshl_add_u64 v[38:39], v[38:39], 0, s[20:21]
	v_lshlrev_b32_e32 v2, 1, v31
	v_pk_mul_f32 v[42:43], v[166:167], v[36:37] op_sel_hi:[1,0]
	s_waitcnt vmcnt(0)
	v_pk_mul_f32 v[40:41], v[24:25], v[40:41]
	v_lshl_add_u64 v[38:39], v[38:39], 0, v[2:3]
	v_pk_mul_f32 v[42:43], v[26:27], v[42:43]
	v_cvt_pk_bf16_f32 v40, v40, v41
	s_nop 0
	v_cvt_pk_bf16_f32 v41, v42, v43
	global_store_dwordx2 v[38:39], v[40:41], off
	v_pk_mul_f32 v[40:41], v[160:161], v[36:37] op_sel_hi:[1,0]
	v_pk_mul_f32 v[42:43], v[162:163], v[36:37] op_sel_hi:[1,0]
	v_pk_mul_f32 v[40:41], v[20:21], v[40:41]
	v_pk_mul_f32 v[42:43], v[22:23], v[42:43]
	v_cvt_pk_bf16_f32 v40, v40, v41
	s_nop 0
	v_cvt_pk_bf16_f32 v41, v42, v43
	global_store_dwordx2 v[38:39], v[40:41], off offset:32
	v_pk_mul_f32 v[40:41], v[156:157], v[36:37] op_sel_hi:[1,0]
	v_pk_mul_f32 v[42:43], v[158:159], v[36:37] op_sel_hi:[1,0]
	v_pk_mul_f32 v[40:41], v[8:9], v[40:41]
	v_pk_mul_f32 v[42:43], v[10:11], v[42:43]
	v_cvt_pk_bf16_f32 v40, v40, v41
	s_nop 0
	v_cvt_pk_bf16_f32 v41, v42, v43
	global_store_dwordx2 v[38:39], v[40:41], off offset:64
	v_pk_mul_f32 v[40:41], v[152:153], v[36:37] op_sel_hi:[1,0]
	v_pk_mul_f32 v[36:37], v[154:155], v[36:37] op_sel_hi:[1,0]
	v_pk_mul_f32 v[40:41], v[4:5], v[40:41]
	v_pk_mul_f32 v[36:37], v[6:7], v[36:37]
	v_cvt_pk_bf16_f32 v40, v40, v41
	v_pk_mul_f32 v[154:155], v[136:137], s[74:75] op_sel_hi:[1,0]
	v_cvt_pk_bf16_f32 v41, v36, v37
	global_store_dwordx2 v[38:39], v[40:41], off offset:96
	v_pk_mul_f32 v[36:37], v[150:151], s[74:75] op_sel_hi:[1,0]
	v_pk_mul_f32 v[38:39], v[148:149], s[74:75] op_sel_hi:[1,0]
	v_pk_mul_f32 v[36:37], v[36:37], v[36:37]
	v_pk_mul_f32 v[38:39], v[38:39], v[38:39]
	v_mul_f32_e32 v1, v154, v154
	v_pk_mov_b32 v[40:41], v[38:39], v[36:37] op_sel:[1,0]
	v_mov_b32_e32 v39, v37
	v_pk_add_f32 v[36:37], v[40:41], v[38:39]
	v_pk_mul_f32 v[38:39], v[146:147], s[74:75] op_sel_hi:[1,0]
	v_pk_mul_f32 v[40:41], v[144:145], s[74:75] op_sel_hi:[1,0]
	v_pk_mul_f32 v[38:39], v[38:39], v[38:39]
	v_pk_mul_f32 v[40:41], v[40:41], v[40:41]
	v_mul_f32_e32 v31, v155, v155
	v_pk_mov_b32 v[42:43], v[40:41], v[38:39] op_sel:[1,0]
	v_mov_b32_e32 v41, v39
	v_pk_add_f32 v[38:39], v[42:43], v[40:41]
	v_pk_add_f32 v[36:37], v[36:37], v[36:37] op_sel:[0,1] op_sel_hi:[1,0]
	v_pk_add_f32 v[38:39], v[38:39], v[38:39] op_sel:[0,1] op_sel_hi:[1,0]
	v_pk_mul_f32 v[42:43], v[140:141], s[74:75] op_sel_hi:[1,0]
	v_mov_b32_e32 v37, v1
	v_mov_b32_e32 v39, v31
	v_pk_mul_f32 v[40:41], v[142:143], s[74:75] op_sel_hi:[1,0]
	v_pk_add_f32 v[36:37], v[36:37], v[38:39]
	v_mul_f32_e32 v38, v43, v43
	v_pk_mul_f32 v[152:153], v[138:139], s[74:75] op_sel_hi:[1,0]
	v_pk_fma_f32 v[38:39], v[42:43], v[42:43], v[38:39] op_sel_hi:[1,1,0]
	v_mul_f32_e32 v42, v41, v41
	v_mul_f32_e32 v35, v152, v152
	v_mul_f32_e32 v152, v153, v153
	v_pk_fma_f32 v[40:41], v[40:41], v[40:41], v[42:43] op_sel_hi:[1,1,0]
	v_mov_b32_e32 v39, v35
	v_mov_b32_e32 v41, v152
	v_pk_add_f32 v[38:39], v[38:39], v[40:41]
	s_nop 0
	v_pk_add_f32 v[36:37], v[36:37], v[38:39]
	s_nop 0
	v_add_f32_e32 v1, v36, v37
	s_waitcnt lgkmcnt(0)
	v_mov_b32_e32 v31, v1
	s_nop 1
	v_permlane16_swap_b32_e32 v31, v1
	v_add_f32_e32 v1, v1, v31
	s_waitcnt lgkmcnt(0)
	v_mov_b32_e32 v31, v1
	s_nop 1
	v_permlane32_swap_b32_e32 v31, v1
	v_add_f32_e32 v1, v1, v31
	v_fmamk_f32 v1, v1, 0x3c800000, v220
	v_cmp_gt_f32_e32 vcc, s93, v1
	v_mul_f32_e32 v31, 0x4f800000, v1
	s_nop 0
	v_cndmask_b32_e32 v1, v1, v31, vcc
	v_sqrt_f32_e32 v31, v1
	s_nop 0
	v_add_u32_e32 v35, -1, v31
	v_fma_f32 v36, -v35, v31, v1
	v_cmp_ge_f32_e64 s[0:1], 0, v36
	v_add_u32_e32 v36, 1, v31
	s_nop 0
	v_cndmask_b32_e64 v35, v31, v35, s[0:1]
	v_fma_f32 v31, -v36, v31, v1
	v_cmp_lt_f32_e64 s[0:1], 0, v31
	s_nop 1
	v_cndmask_b32_e64 v31, v35, v36, s[0:1]
	v_mul_f32_e32 v35, 0x37800000, v31
	v_cndmask_b32_e32 v31, v31, v35, vcc
	v_cmp_class_f32_e32 vcc, v1, v221
	s_nop 1
	v_cndmask_b32_e32 v1, v31, v1, vcc
	v_div_scale_f32 v31, s[0:1], v1, v1, v32
	v_rcp_f32_e32 v35, v31
	s_nop 0
	v_fma_f32 v36, -v31, v35, 1.0
	v_fmac_f32_e32 v35, v36, v35
	v_div_scale_f32 v36, vcc, v32, v1, v32
	v_mul_f32_e32 v37, v36, v35
	v_fma_f32 v38, -v31, v37, v36
	v_fmac_f32_e32 v37, v38, v35
	v_fma_f32 v31, -v31, v37, v36
	v_div_fmas_f32 v31, v31, v35, v37
	v_div_fixup_f32 v36, v31, v1, v32
	v_or_b32_e32 v1, 16, v30
	v_mad_i64_i32 v[38:39], s[0:1], v1, s96, v[28:29]
	v_lshl_add_u64 v[38:39], v[38:39], 0, s[72:73]
	v_pk_mul_f32 v[40:41], v[148:149], v[36:37] op_sel_hi:[1,0]
	v_lshl_add_u64 v[38:39], v[38:39], 0, s[20:21]
	v_pk_mul_f32 v[42:43], v[150:151], v[36:37] op_sel_hi:[1,0]
	v_pk_mul_f32 v[40:41], v[24:25], v[40:41]
	v_lshl_add_u64 v[38:39], v[38:39], 0, v[2:3]
	v_pk_mul_f32 v[42:43], v[26:27], v[42:43]
	v_cvt_pk_bf16_f32 v40, v40, v41
	s_nop 0
	v_cvt_pk_bf16_f32 v41, v42, v43
	global_store_dwordx2 v[38:39], v[40:41], off
	v_pk_mul_f32 v[40:41], v[144:145], v[36:37] op_sel_hi:[1,0]
	v_pk_mul_f32 v[42:43], v[146:147], v[36:37] op_sel_hi:[1,0]
	v_pk_mul_f32 v[40:41], v[20:21], v[40:41]
	v_pk_mul_f32 v[42:43], v[22:23], v[42:43]
	v_cvt_pk_bf16_f32 v40, v40, v41
	s_nop 0
	v_cvt_pk_bf16_f32 v41, v42, v43
	global_store_dwordx2 v[38:39], v[40:41], off offset:32
	v_pk_mul_f32 v[40:41], v[140:141], v[36:37] op_sel_hi:[1,0]
	v_pk_mul_f32 v[42:43], v[142:143], v[36:37] op_sel_hi:[1,0]
	v_pk_mul_f32 v[40:41], v[8:9], v[40:41]
	v_pk_mul_f32 v[42:43], v[10:11], v[42:43]
	v_cvt_pk_bf16_f32 v40, v40, v41
	s_nop 0
	v_cvt_pk_bf16_f32 v41, v42, v43
	global_store_dwordx2 v[38:39], v[40:41], off offset:64
	v_pk_mul_f32 v[40:41], v[136:137], v[36:37] op_sel_hi:[1,0]
	v_pk_mul_f32 v[36:37], v[138:139], v[36:37] op_sel_hi:[1,0]
	v_pk_mul_f32 v[40:41], v[4:5], v[40:41]
	v_pk_mul_f32 v[36:37], v[6:7], v[36:37]
	v_cvt_pk_bf16_f32 v40, v40, v41
	v_pk_mul_f32 v[138:139], v[120:121], s[74:75] op_sel_hi:[1,0]
	v_cvt_pk_bf16_f32 v41, v36, v37
	global_store_dwordx2 v[38:39], v[40:41], off offset:96
	v_pk_mul_f32 v[36:37], v[134:135], s[74:75] op_sel_hi:[1,0]
	v_pk_mul_f32 v[38:39], v[132:133], s[74:75] op_sel_hi:[1,0]
	v_pk_mul_f32 v[36:37], v[36:37], v[36:37]
	v_pk_mul_f32 v[38:39], v[38:39], v[38:39]
	v_mul_f32_e32 v1, v138, v138
	v_pk_mov_b32 v[40:41], v[38:39], v[36:37] op_sel:[1,0]
	v_mov_b32_e32 v39, v37
	v_pk_add_f32 v[36:37], v[40:41], v[38:39]
	v_pk_mul_f32 v[38:39], v[130:131], s[74:75] op_sel_hi:[1,0]
	v_pk_mul_f32 v[40:41], v[128:129], s[74:75] op_sel_hi:[1,0]
	v_pk_mul_f32 v[38:39], v[38:39], v[38:39]
	v_pk_mul_f32 v[40:41], v[40:41], v[40:41]
	v_mul_f32_e32 v31, v139, v139
	v_pk_mov_b32 v[42:43], v[40:41], v[38:39] op_sel:[1,0]
	v_mov_b32_e32 v41, v39
	v_pk_add_f32 v[38:39], v[42:43], v[40:41]
	v_pk_add_f32 v[36:37], v[36:37], v[36:37] op_sel:[0,1] op_sel_hi:[1,0]
	v_pk_add_f32 v[38:39], v[38:39], v[38:39] op_sel:[0,1] op_sel_hi:[1,0]
	v_pk_mul_f32 v[42:43], v[124:125], s[74:75] op_sel_hi:[1,0]
	v_mov_b32_e32 v37, v1
	v_mov_b32_e32 v39, v31
	v_pk_mul_f32 v[40:41], v[126:127], s[74:75] op_sel_hi:[1,0]
	v_pk_add_f32 v[36:37], v[36:37], v[38:39]
	v_mul_f32_e32 v38, v43, v43
	v_pk_mul_f32 v[136:137], v[122:123], s[74:75] op_sel_hi:[1,0]
	v_pk_fma_f32 v[38:39], v[42:43], v[42:43], v[38:39] op_sel_hi:[1,1,0]
	v_mul_f32_e32 v42, v41, v41
	v_mul_f32_e32 v35, v136, v136
	v_mul_f32_e32 v136, v137, v137
	v_pk_fma_f32 v[40:41], v[40:41], v[40:41], v[42:43] op_sel_hi:[1,1,0]
	v_mov_b32_e32 v39, v35
	v_mov_b32_e32 v41, v136
	v_pk_add_f32 v[38:39], v[38:39], v[40:41]
	s_nop 0
	v_pk_add_f32 v[36:37], v[36:37], v[38:39]
	s_nop 0
	v_add_f32_e32 v1, v36, v37
	s_waitcnt lgkmcnt(0)
	v_mov_b32_e32 v31, v1
	s_nop 1
	v_permlane16_swap_b32_e32 v31, v1
	v_add_f32_e32 v1, v1, v31
	s_waitcnt lgkmcnt(0)
	v_mov_b32_e32 v31, v1
	s_nop 1
	v_permlane32_swap_b32_e32 v31, v1
	v_add_f32_e32 v1, v1, v31
	v_fmamk_f32 v1, v1, 0x3c800000, v220
	v_cmp_gt_f32_e32 vcc, s93, v1
	v_mul_f32_e32 v31, 0x4f800000, v1
	s_nop 0
	v_cndmask_b32_e32 v1, v1, v31, vcc
	v_sqrt_f32_e32 v31, v1
	s_nop 0
	v_add_u32_e32 v35, -1, v31
	v_fma_f32 v36, -v35, v31, v1
	v_cmp_ge_f32_e64 s[0:1], 0, v36
	v_add_u32_e32 v36, 1, v31
	s_nop 0
	v_cndmask_b32_e64 v35, v31, v35, s[0:1]
	v_fma_f32 v31, -v36, v31, v1
	v_cmp_lt_f32_e64 s[0:1], 0, v31
	s_nop 1
	v_cndmask_b32_e64 v31, v35, v36, s[0:1]
	v_mul_f32_e32 v35, 0x37800000, v31
	v_cndmask_b32_e32 v31, v31, v35, vcc
	v_cmp_class_f32_e32 vcc, v1, v221
	s_nop 1
	v_cndmask_b32_e32 v1, v31, v1, vcc
	v_div_scale_f32 v31, s[0:1], v1, v1, v32
	v_rcp_f32_e32 v35, v31
	s_nop 0
	v_fma_f32 v36, -v31, v35, 1.0
	v_fmac_f32_e32 v35, v36, v35
	v_div_scale_f32 v36, vcc, v32, v1, v32
	v_mul_f32_e32 v37, v36, v35
	v_fma_f32 v38, -v31, v37, v36
	v_fmac_f32_e32 v37, v38, v35
	v_fma_f32 v31, -v31, v37, v36
	v_div_fmas_f32 v31, v31, v35, v37
	v_div_fixup_f32 v36, v31, v1, v32
	v_or_b32_e32 v1, 32, v30
	v_mad_i64_i32 v[38:39], s[0:1], v1, s96, v[28:29]
	v_lshl_add_u64 v[38:39], v[38:39], 0, s[72:73]
	v_pk_mul_f32 v[40:41], v[132:133], v[36:37] op_sel_hi:[1,0]
	v_lshl_add_u64 v[38:39], v[38:39], 0, s[20:21]
	v_pk_mul_f32 v[42:43], v[134:135], v[36:37] op_sel_hi:[1,0]
	v_pk_mul_f32 v[40:41], v[24:25], v[40:41]
	v_lshl_add_u64 v[38:39], v[38:39], 0, v[2:3]
	v_pk_mul_f32 v[42:43], v[26:27], v[42:43]
	v_cvt_pk_bf16_f32 v40, v40, v41
	s_nop 0
	v_cvt_pk_bf16_f32 v41, v42, v43
	global_store_dwordx2 v[38:39], v[40:41], off
	v_pk_mul_f32 v[40:41], v[128:129], v[36:37] op_sel_hi:[1,0]
	v_pk_mul_f32 v[42:43], v[130:131], v[36:37] op_sel_hi:[1,0]
	v_pk_mul_f32 v[40:41], v[20:21], v[40:41]
	v_pk_mul_f32 v[42:43], v[22:23], v[42:43]
	v_cvt_pk_bf16_f32 v40, v40, v41
	s_nop 0
	v_cvt_pk_bf16_f32 v41, v42, v43
	global_store_dwordx2 v[38:39], v[40:41], off offset:32
	v_pk_mul_f32 v[40:41], v[124:125], v[36:37] op_sel_hi:[1,0]
	v_pk_mul_f32 v[42:43], v[126:127], v[36:37] op_sel_hi:[1,0]
	v_pk_mul_f32 v[40:41], v[8:9], v[40:41]
	v_pk_mul_f32 v[42:43], v[10:11], v[42:43]
	v_cvt_pk_bf16_f32 v40, v40, v41
	s_nop 0
	v_cvt_pk_bf16_f32 v41, v42, v43
	global_store_dwordx2 v[38:39], v[40:41], off offset:64
	v_pk_mul_f32 v[40:41], v[120:121], v[36:37] op_sel_hi:[1,0]
	v_pk_mul_f32 v[36:37], v[122:123], v[36:37] op_sel_hi:[1,0]
	v_pk_mul_f32 v[40:41], v[4:5], v[40:41]
	v_pk_mul_f32 v[36:37], v[6:7], v[36:37]
	v_cvt_pk_bf16_f32 v40, v40, v41
	v_pk_mul_f32 v[122:123], v[104:105], s[74:75] op_sel_hi:[1,0]
	v_cvt_pk_bf16_f32 v41, v36, v37
	global_store_dwordx2 v[38:39], v[40:41], off offset:96
	v_pk_mul_f32 v[36:37], v[118:119], s[74:75] op_sel_hi:[1,0]
	v_pk_mul_f32 v[38:39], v[116:117], s[74:75] op_sel_hi:[1,0]
	v_pk_mul_f32 v[36:37], v[36:37], v[36:37]
	v_pk_mul_f32 v[38:39], v[38:39], v[38:39]
	v_mul_f32_e32 v1, v122, v122
	v_pk_mov_b32 v[40:41], v[38:39], v[36:37] op_sel:[1,0]
	v_mov_b32_e32 v39, v37
	v_pk_add_f32 v[36:37], v[40:41], v[38:39]
	v_pk_mul_f32 v[38:39], v[114:115], s[74:75] op_sel_hi:[1,0]
	v_pk_mul_f32 v[40:41], v[112:113], s[74:75] op_sel_hi:[1,0]
	v_pk_mul_f32 v[38:39], v[38:39], v[38:39]
	v_pk_mul_f32 v[40:41], v[40:41], v[40:41]
	v_mul_f32_e32 v31, v123, v123
	v_pk_mov_b32 v[42:43], v[40:41], v[38:39] op_sel:[1,0]
	v_mov_b32_e32 v41, v39
	v_pk_add_f32 v[38:39], v[42:43], v[40:41]
	v_pk_add_f32 v[36:37], v[36:37], v[36:37] op_sel:[0,1] op_sel_hi:[1,0]
	v_pk_add_f32 v[38:39], v[38:39], v[38:39] op_sel:[0,1] op_sel_hi:[1,0]
	v_pk_mul_f32 v[42:43], v[108:109], s[74:75] op_sel_hi:[1,0]
	v_mov_b32_e32 v37, v1
	v_mov_b32_e32 v39, v31
	v_pk_mul_f32 v[40:41], v[110:111], s[74:75] op_sel_hi:[1,0]
	v_pk_add_f32 v[36:37], v[36:37], v[38:39]
	v_mul_f32_e32 v38, v43, v43
	v_pk_mul_f32 v[120:121], v[106:107], s[74:75] op_sel_hi:[1,0]
	v_pk_fma_f32 v[38:39], v[42:43], v[42:43], v[38:39] op_sel_hi:[1,1,0]
	v_mul_f32_e32 v42, v41, v41
	v_mul_f32_e32 v35, v120, v120
	v_mul_f32_e32 v120, v121, v121
	v_pk_fma_f32 v[40:41], v[40:41], v[40:41], v[42:43] op_sel_hi:[1,1,0]
	v_mov_b32_e32 v39, v35
	v_mov_b32_e32 v41, v120
	v_pk_add_f32 v[38:39], v[38:39], v[40:41]
	s_nop 0
	v_pk_add_f32 v[36:37], v[36:37], v[38:39]
	s_nop 0
	v_add_f32_e32 v1, v36, v37
	s_waitcnt lgkmcnt(0)
	v_mov_b32_e32 v31, v1
	s_nop 1
	v_permlane16_swap_b32_e32 v31, v1
	v_add_f32_e32 v1, v1, v31
	s_waitcnt lgkmcnt(0)
	v_mov_b32_e32 v31, v1
	s_nop 1
	v_permlane32_swap_b32_e32 v31, v1
	v_add_f32_e32 v1, v1, v31
	v_fmamk_f32 v1, v1, 0x3c800000, v220
	v_cmp_gt_f32_e32 vcc, s93, v1
	v_mul_f32_e32 v31, 0x4f800000, v1
	s_nop 0
	v_cndmask_b32_e32 v1, v1, v31, vcc
	v_sqrt_f32_e32 v31, v1
	s_nop 0
	v_add_u32_e32 v35, -1, v31
	v_fma_f32 v36, -v35, v31, v1
	v_cmp_ge_f32_e64 s[0:1], 0, v36
	v_add_u32_e32 v36, 1, v31
	s_nop 0
	v_cndmask_b32_e64 v35, v31, v35, s[0:1]
	v_fma_f32 v31, -v36, v31, v1
	v_cmp_lt_f32_e64 s[0:1], 0, v31
	s_nop 1
	v_cndmask_b32_e64 v31, v35, v36, s[0:1]
	v_mul_f32_e32 v35, 0x37800000, v31
	v_cndmask_b32_e32 v31, v31, v35, vcc
	v_cmp_class_f32_e32 vcc, v1, v221
	s_nop 1
	v_cndmask_b32_e32 v1, v31, v1, vcc
	v_div_scale_f32 v31, s[0:1], v1, v1, v32
	v_rcp_f32_e32 v35, v31
	s_nop 0
	v_fma_f32 v36, -v31, v35, 1.0
	v_fmac_f32_e32 v35, v36, v35
	v_div_scale_f32 v36, vcc, v32, v1, v32
	v_mul_f32_e32 v37, v36, v35
	v_fma_f32 v38, -v31, v37, v36
	v_fmac_f32_e32 v37, v38, v35
	v_fma_f32 v31, -v31, v37, v36
	v_div_fmas_f32 v31, v31, v35, v37
	v_div_fixup_f32 v36, v31, v1, v32
	v_or_b32_e32 v1, 48, v30
	v_mad_i64_i32 v[38:39], s[0:1], v1, s96, v[28:29]
	v_lshl_add_u64 v[38:39], v[38:39], 0, s[72:73]
	v_pk_mul_f32 v[40:41], v[116:117], v[36:37] op_sel_hi:[1,0]
	v_lshl_add_u64 v[38:39], v[38:39], 0, s[20:21]
	v_pk_mul_f32 v[42:43], v[118:119], v[36:37] op_sel_hi:[1,0]
	v_pk_mul_f32 v[40:41], v[24:25], v[40:41]
	v_lshl_add_u64 v[38:39], v[38:39], 0, v[2:3]
	v_pk_mul_f32 v[42:43], v[26:27], v[42:43]
	v_cvt_pk_bf16_f32 v40, v40, v41
	v_add_u32_e32 v1, 0x80, v30
	v_cvt_pk_bf16_f32 v41, v42, v43
	global_store_dwordx2 v[38:39], v[40:41], off
	v_pk_mul_f32 v[40:41], v[112:113], v[36:37] op_sel_hi:[1,0]
	v_pk_mul_f32 v[42:43], v[114:115], v[36:37] op_sel_hi:[1,0]
	v_pk_mul_f32 v[40:41], v[20:21], v[40:41]
	v_pk_mul_f32 v[42:43], v[22:23], v[42:43]
	v_cvt_pk_bf16_f32 v40, v40, v41
	s_nop 0
	v_cvt_pk_bf16_f32 v41, v42, v43
	global_store_dwordx2 v[38:39], v[40:41], off offset:32
	v_pk_mul_f32 v[40:41], v[108:109], v[36:37] op_sel_hi:[1,0]
	v_pk_mul_f32 v[42:43], v[110:111], v[36:37] op_sel_hi:[1,0]
	v_pk_mul_f32 v[40:41], v[8:9], v[40:41]
	v_pk_mul_f32 v[42:43], v[10:11], v[42:43]
	v_cvt_pk_bf16_f32 v40, v40, v41
	s_nop 0
	v_cvt_pk_bf16_f32 v41, v42, v43
	global_store_dwordx2 v[38:39], v[40:41], off offset:64
	v_pk_mul_f32 v[40:41], v[104:105], v[36:37] op_sel_hi:[1,0]
	v_pk_mul_f32 v[36:37], v[106:107], v[36:37] op_sel_hi:[1,0]
	v_pk_mul_f32 v[40:41], v[4:5], v[40:41]
	v_pk_mul_f32 v[36:37], v[6:7], v[36:37]
	v_cvt_pk_bf16_f32 v40, v40, v41
	v_pk_mul_f32 v[106:107], v[88:89], s[74:75] op_sel_hi:[1,0]
	v_cvt_pk_bf16_f32 v41, v36, v37
	global_store_dwordx2 v[38:39], v[40:41], off offset:96
	v_pk_mul_f32 v[36:37], v[102:103], s[74:75] op_sel_hi:[1,0]
	v_pk_mul_f32 v[38:39], v[100:101], s[74:75] op_sel_hi:[1,0]
	v_pk_mul_f32 v[36:37], v[36:37], v[36:37]
	v_pk_mul_f32 v[38:39], v[38:39], v[38:39]
	v_mul_f32_e32 v31, v106, v106
	v_pk_mov_b32 v[40:41], v[38:39], v[36:37] op_sel:[1,0]
	v_mov_b32_e32 v39, v37
	v_pk_add_f32 v[36:37], v[40:41], v[38:39]
	v_pk_mul_f32 v[38:39], v[98:99], s[74:75] op_sel_hi:[1,0]
	v_pk_mul_f32 v[40:41], v[96:97], s[74:75] op_sel_hi:[1,0]
	v_pk_mul_f32 v[38:39], v[38:39], v[38:39]
	v_pk_mul_f32 v[40:41], v[40:41], v[40:41]
	v_mul_f32_e32 v35, v107, v107
	v_pk_mov_b32 v[42:43], v[40:41], v[38:39] op_sel:[1,0]
	v_mov_b32_e32 v41, v39
	v_pk_add_f32 v[38:39], v[42:43], v[40:41]
	v_pk_add_f32 v[36:37], v[36:37], v[36:37] op_sel:[0,1] op_sel_hi:[1,0]
	v_pk_add_f32 v[38:39], v[38:39], v[38:39] op_sel:[0,1] op_sel_hi:[1,0]
	v_pk_mul_f32 v[42:43], v[92:93], s[74:75] op_sel_hi:[1,0]
	v_mov_b32_e32 v37, v31
	v_mov_b32_e32 v39, v35
	v_pk_mul_f32 v[40:41], v[94:95], s[74:75] op_sel_hi:[1,0]
	v_pk_add_f32 v[36:37], v[36:37], v[38:39]
	v_mul_f32_e32 v38, v43, v43
	v_pk_mul_f32 v[104:105], v[90:91], s[74:75] op_sel_hi:[1,0]
	v_pk_fma_f32 v[38:39], v[42:43], v[42:43], v[38:39] op_sel_hi:[1,1,0]
	v_mul_f32_e32 v42, v41, v41
	v_mul_f32_e32 v104, v104, v104
	v_mul_f32_e32 v105, v105, v105
	v_pk_fma_f32 v[40:41], v[40:41], v[40:41], v[42:43] op_sel_hi:[1,1,0]
	v_mov_b32_e32 v39, v104
	v_mov_b32_e32 v41, v105
	v_pk_add_f32 v[38:39], v[38:39], v[40:41]
	s_nop 0
	v_pk_add_f32 v[36:37], v[36:37], v[38:39]
	s_nop 0
	v_add_f32_e32 v31, v36, v37
	s_waitcnt lgkmcnt(0)
	v_mov_b32_e32 v35, v31
	s_nop 1
	v_permlane16_swap_b32_e32 v35, v31
	v_add_f32_e32 v31, v31, v35
	s_waitcnt lgkmcnt(0)
	v_mov_b32_e32 v35, v31
	s_nop 1
	v_permlane32_swap_b32_e32 v35, v31
	v_add_f32_e32 v31, v31, v35
	v_fmamk_f32 v31, v31, 0x3c800000, v220
	v_cmp_gt_f32_e32 vcc, s93, v31
	v_mul_f32_e32 v35, 0x4f800000, v31
	s_nop 0
	v_cndmask_b32_e32 v31, v31, v35, vcc
	v_sqrt_f32_e32 v35, v31
	s_nop 0
	v_add_u32_e32 v36, -1, v35
	v_fma_f32 v37, -v36, v35, v31
	v_cmp_ge_f32_e64 s[0:1], 0, v37
	v_add_u32_e32 v37, 1, v35
	s_nop 0
	v_cndmask_b32_e64 v36, v35, v36, s[0:1]
	v_fma_f32 v35, -v37, v35, v31
	v_cmp_lt_f32_e64 s[0:1], 0, v35
	s_nop 1
	v_cndmask_b32_e64 v35, v36, v37, s[0:1]
	v_mul_f32_e32 v36, 0x37800000, v35
	v_cndmask_b32_e32 v35, v35, v36, vcc
	v_cmp_class_f32_e32 vcc, v31, v221
	s_nop 1
	v_cndmask_b32_e32 v31, v35, v31, vcc
	v_div_scale_f32 v35, s[0:1], v31, v31, v32
	v_rcp_f32_e32 v36, v35
	s_nop 0
	v_fma_f32 v37, -v35, v36, 1.0
	v_fmac_f32_e32 v36, v37, v36
	v_div_scale_f32 v37, vcc, v32, v31, v32
	v_mul_f32_e32 v38, v37, v36
	v_fma_f32 v39, -v35, v38, v37
	v_fmac_f32_e32 v38, v39, v36
	v_fma_f32 v35, -v35, v38, v37
	v_div_fmas_f32 v35, v35, v36, v38
	v_div_fixup_f32 v36, v35, v31, v32
	v_mad_i64_i32 v[38:39], s[0:1], v1, s96, v[28:29]
	v_lshl_add_u64 v[38:39], v[38:39], 0, s[72:73]
	v_pk_mul_f32 v[40:41], v[100:101], v[36:37] op_sel_hi:[1,0]
	v_lshl_add_u64 v[38:39], v[38:39], 0, s[20:21]
	v_pk_mul_f32 v[42:43], v[102:103], v[36:37] op_sel_hi:[1,0]
	v_pk_mul_f32 v[40:41], v[24:25], v[40:41]
	v_lshl_add_u64 v[38:39], v[38:39], 0, v[2:3]
	v_pk_mul_f32 v[42:43], v[26:27], v[42:43]
	v_cvt_pk_bf16_f32 v40, v40, v41
	s_nop 0
	v_cvt_pk_bf16_f32 v41, v42, v43
	global_store_dwordx2 v[38:39], v[40:41], off
	v_pk_mul_f32 v[40:41], v[96:97], v[36:37] op_sel_hi:[1,0]
	v_pk_mul_f32 v[42:43], v[98:99], v[36:37] op_sel_hi:[1,0]
	v_pk_mul_f32 v[40:41], v[20:21], v[40:41]
	v_pk_mul_f32 v[42:43], v[22:23], v[42:43]
	v_cvt_pk_bf16_f32 v40, v40, v41
	s_nop 0
	v_cvt_pk_bf16_f32 v41, v42, v43
	global_store_dwordx2 v[38:39], v[40:41], off offset:32
	v_pk_mul_f32 v[40:41], v[92:93], v[36:37] op_sel_hi:[1,0]
	v_pk_mul_f32 v[42:43], v[94:95], v[36:37] op_sel_hi:[1,0]
	v_pk_mul_f32 v[40:41], v[8:9], v[40:41]
	v_pk_mul_f32 v[42:43], v[10:11], v[42:43]
	v_cvt_pk_bf16_f32 v40, v40, v41
	s_nop 0
	v_cvt_pk_bf16_f32 v41, v42, v43
	global_store_dwordx2 v[38:39], v[40:41], off offset:64
	v_pk_mul_f32 v[40:41], v[88:89], v[36:37] op_sel_hi:[1,0]
	v_pk_mul_f32 v[36:37], v[90:91], v[36:37] op_sel_hi:[1,0]
	v_pk_mul_f32 v[40:41], v[4:5], v[40:41]
	v_pk_mul_f32 v[36:37], v[6:7], v[36:37]
	v_cvt_pk_bf16_f32 v40, v40, v41
	v_pk_mul_f32 v[90:91], v[72:73], s[74:75] op_sel_hi:[1,0]
	v_cvt_pk_bf16_f32 v41, v36, v37
	global_store_dwordx2 v[38:39], v[40:41], off offset:96
	v_pk_mul_f32 v[36:37], v[86:87], s[74:75] op_sel_hi:[1,0]
	v_pk_mul_f32 v[38:39], v[84:85], s[74:75] op_sel_hi:[1,0]
	v_pk_mul_f32 v[36:37], v[36:37], v[36:37]
	v_pk_mul_f32 v[38:39], v[38:39], v[38:39]
	v_mul_f32_e32 v1, v90, v90
	v_pk_mov_b32 v[40:41], v[38:39], v[36:37] op_sel:[1,0]
	v_mov_b32_e32 v39, v37
	v_pk_add_f32 v[36:37], v[40:41], v[38:39]
	v_pk_mul_f32 v[38:39], v[82:83], s[74:75] op_sel_hi:[1,0]
	v_pk_mul_f32 v[40:41], v[80:81], s[74:75] op_sel_hi:[1,0]
	v_pk_mul_f32 v[38:39], v[38:39], v[38:39]
	v_pk_mul_f32 v[40:41], v[40:41], v[40:41]
	v_mul_f32_e32 v31, v91, v91
	v_pk_mov_b32 v[42:43], v[40:41], v[38:39] op_sel:[1,0]
	v_mov_b32_e32 v41, v39
	v_pk_add_f32 v[38:39], v[42:43], v[40:41]
	v_pk_add_f32 v[36:37], v[36:37], v[36:37] op_sel:[0,1] op_sel_hi:[1,0]
	v_pk_add_f32 v[38:39], v[38:39], v[38:39] op_sel:[0,1] op_sel_hi:[1,0]
	v_pk_mul_f32 v[42:43], v[76:77], s[74:75] op_sel_hi:[1,0]
	v_mov_b32_e32 v37, v1
	v_mov_b32_e32 v39, v31
	v_pk_mul_f32 v[40:41], v[78:79], s[74:75] op_sel_hi:[1,0]
	v_pk_add_f32 v[36:37], v[36:37], v[38:39]
	v_mul_f32_e32 v38, v43, v43
	v_pk_mul_f32 v[88:89], v[74:75], s[74:75] op_sel_hi:[1,0]
	v_pk_fma_f32 v[38:39], v[42:43], v[42:43], v[38:39] op_sel_hi:[1,1,0]
	v_mul_f32_e32 v42, v41, v41
	v_mul_f32_e32 v35, v88, v88
	v_mul_f32_e32 v88, v89, v89
	v_pk_fma_f32 v[40:41], v[40:41], v[40:41], v[42:43] op_sel_hi:[1,1,0]
	v_mov_b32_e32 v39, v35
	v_mov_b32_e32 v41, v88
	v_pk_add_f32 v[38:39], v[38:39], v[40:41]
	s_nop 0
	v_pk_add_f32 v[36:37], v[36:37], v[38:39]
	s_nop 0
	v_add_f32_e32 v1, v36, v37
	s_waitcnt lgkmcnt(0)
	v_mov_b32_e32 v31, v1
	s_nop 1
	v_permlane16_swap_b32_e32 v31, v1
	v_add_f32_e32 v1, v1, v31
	s_waitcnt lgkmcnt(0)
	v_mov_b32_e32 v31, v1
	s_nop 1
	v_permlane32_swap_b32_e32 v31, v1
	v_add_f32_e32 v1, v1, v31
	v_fmamk_f32 v1, v1, 0x3c800000, v220
	v_cmp_gt_f32_e32 vcc, s93, v1
	v_mul_f32_e32 v31, 0x4f800000, v1
	s_nop 0
	v_cndmask_b32_e32 v1, v1, v31, vcc
	v_sqrt_f32_e32 v31, v1
	s_nop 0
	v_add_u32_e32 v35, -1, v31
	v_fma_f32 v36, -v35, v31, v1
	v_cmp_ge_f32_e64 s[0:1], 0, v36
	v_add_u32_e32 v36, 1, v31
	s_nop 0
	v_cndmask_b32_e64 v35, v31, v35, s[0:1]
	v_fma_f32 v31, -v36, v31, v1
	v_cmp_lt_f32_e64 s[0:1], 0, v31
	s_nop 1
	v_cndmask_b32_e64 v31, v35, v36, s[0:1]
	v_mul_f32_e32 v35, 0x37800000, v31
	v_cndmask_b32_e32 v31, v31, v35, vcc
	v_cmp_class_f32_e32 vcc, v1, v221
	s_nop 1
	v_cndmask_b32_e32 v1, v31, v1, vcc
	v_div_scale_f32 v31, s[0:1], v1, v1, v32
	v_rcp_f32_e32 v35, v31
	s_nop 0
	v_fma_f32 v36, -v31, v35, 1.0
	v_fmac_f32_e32 v35, v36, v35
	v_div_scale_f32 v36, vcc, v32, v1, v32
	v_mul_f32_e32 v37, v36, v35
	v_fma_f32 v38, -v31, v37, v36
	v_fmac_f32_e32 v37, v38, v35
	v_fma_f32 v31, -v31, v37, v36
	v_div_fmas_f32 v31, v31, v35, v37
	v_div_fixup_f32 v36, v31, v1, v32
	v_add_u32_e32 v1, 0x90, v30
	v_mad_i64_i32 v[38:39], s[0:1], v1, s96, v[28:29]
	v_lshl_add_u64 v[38:39], v[38:39], 0, s[72:73]
	v_pk_mul_f32 v[40:41], v[84:85], v[36:37] op_sel_hi:[1,0]
	v_lshl_add_u64 v[38:39], v[38:39], 0, s[20:21]
	v_pk_mul_f32 v[42:43], v[86:87], v[36:37] op_sel_hi:[1,0]
	v_pk_mul_f32 v[40:41], v[24:25], v[40:41]
	v_lshl_add_u64 v[38:39], v[38:39], 0, v[2:3]
	v_pk_mul_f32 v[42:43], v[26:27], v[42:43]
	v_cvt_pk_bf16_f32 v40, v40, v41
	s_nop 0
	v_cvt_pk_bf16_f32 v41, v42, v43
	global_store_dwordx2 v[38:39], v[40:41], off
	v_pk_mul_f32 v[40:41], v[80:81], v[36:37] op_sel_hi:[1,0]
	v_pk_mul_f32 v[42:43], v[82:83], v[36:37] op_sel_hi:[1,0]
	v_pk_mul_f32 v[40:41], v[20:21], v[40:41]
	v_pk_mul_f32 v[42:43], v[22:23], v[42:43]
	v_cvt_pk_bf16_f32 v40, v40, v41
	s_nop 0
	v_cvt_pk_bf16_f32 v41, v42, v43
	global_store_dwordx2 v[38:39], v[40:41], off offset:32
	v_pk_mul_f32 v[40:41], v[76:77], v[36:37] op_sel_hi:[1,0]
	v_pk_mul_f32 v[42:43], v[78:79], v[36:37] op_sel_hi:[1,0]
	v_pk_mul_f32 v[40:41], v[8:9], v[40:41]
	v_pk_mul_f32 v[42:43], v[10:11], v[42:43]
	v_cvt_pk_bf16_f32 v40, v40, v41
	s_nop 0
	v_cvt_pk_bf16_f32 v41, v42, v43
	global_store_dwordx2 v[38:39], v[40:41], off offset:64
	v_pk_mul_f32 v[40:41], v[72:73], v[36:37] op_sel_hi:[1,0]
	v_pk_mul_f32 v[36:37], v[74:75], v[36:37] op_sel_hi:[1,0]
	v_pk_mul_f32 v[40:41], v[4:5], v[40:41]
	v_pk_mul_f32 v[36:37], v[6:7], v[36:37]
	v_cvt_pk_bf16_f32 v40, v40, v41
	v_pk_mul_f32 v[74:75], v[56:57], s[74:75] op_sel_hi:[1,0]
	v_cvt_pk_bf16_f32 v41, v36, v37
	global_store_dwordx2 v[38:39], v[40:41], off offset:96
	v_pk_mul_f32 v[36:37], v[70:71], s[74:75] op_sel_hi:[1,0]
	v_pk_mul_f32 v[38:39], v[68:69], s[74:75] op_sel_hi:[1,0]
	v_pk_mul_f32 v[36:37], v[36:37], v[36:37]
	v_pk_mul_f32 v[38:39], v[38:39], v[38:39]
	v_mul_f32_e32 v1, v74, v74
	v_pk_mov_b32 v[40:41], v[38:39], v[36:37] op_sel:[1,0]
	v_mov_b32_e32 v39, v37
	v_pk_add_f32 v[36:37], v[40:41], v[38:39]
	v_pk_mul_f32 v[38:39], v[66:67], s[74:75] op_sel_hi:[1,0]
	v_pk_mul_f32 v[40:41], v[64:65], s[74:75] op_sel_hi:[1,0]
	v_pk_mul_f32 v[38:39], v[38:39], v[38:39]
	v_pk_mul_f32 v[40:41], v[40:41], v[40:41]
	v_mul_f32_e32 v31, v75, v75
	v_pk_mov_b32 v[42:43], v[40:41], v[38:39] op_sel:[1,0]
	v_mov_b32_e32 v41, v39
	v_pk_add_f32 v[38:39], v[42:43], v[40:41]
	v_pk_add_f32 v[36:37], v[36:37], v[36:37] op_sel:[0,1] op_sel_hi:[1,0]
	v_pk_add_f32 v[38:39], v[38:39], v[38:39] op_sel:[0,1] op_sel_hi:[1,0]
	v_pk_mul_f32 v[42:43], v[60:61], s[74:75] op_sel_hi:[1,0]
	v_mov_b32_e32 v37, v1
	v_mov_b32_e32 v39, v31
	v_pk_mul_f32 v[40:41], v[62:63], s[74:75] op_sel_hi:[1,0]
	v_pk_add_f32 v[36:37], v[36:37], v[38:39]
	v_mul_f32_e32 v38, v43, v43
	v_pk_mul_f32 v[72:73], v[58:59], s[74:75] op_sel_hi:[1,0]
	v_pk_fma_f32 v[38:39], v[42:43], v[42:43], v[38:39] op_sel_hi:[1,1,0]
	v_mul_f32_e32 v42, v41, v41
	v_mul_f32_e32 v35, v72, v72
	v_mul_f32_e32 v72, v73, v73
	v_pk_fma_f32 v[40:41], v[40:41], v[40:41], v[42:43] op_sel_hi:[1,1,0]
	v_mov_b32_e32 v39, v35
	v_mov_b32_e32 v41, v72
	v_pk_add_f32 v[38:39], v[38:39], v[40:41]
	s_nop 0
	v_pk_add_f32 v[36:37], v[36:37], v[38:39]
	s_nop 0
	v_add_f32_e32 v1, v36, v37
	s_waitcnt lgkmcnt(0)
	v_mov_b32_e32 v31, v1
	s_nop 1
	v_permlane16_swap_b32_e32 v31, v1
	v_add_f32_e32 v1, v1, v31
	s_waitcnt lgkmcnt(0)
	v_mov_b32_e32 v31, v1
	s_nop 1
	v_permlane32_swap_b32_e32 v31, v1
	v_add_f32_e32 v1, v1, v31
	v_fmamk_f32 v1, v1, 0x3c800000, v220
	v_cmp_gt_f32_e32 vcc, s93, v1
	v_mul_f32_e32 v31, 0x4f800000, v1
	s_nop 0
	v_cndmask_b32_e32 v1, v1, v31, vcc
	v_sqrt_f32_e32 v31, v1
	s_nop 0
	v_add_u32_e32 v35, -1, v31
	v_fma_f32 v36, -v35, v31, v1
	v_cmp_ge_f32_e64 s[0:1], 0, v36
	v_add_u32_e32 v36, 1, v31
	s_nop 0
	v_cndmask_b32_e64 v35, v31, v35, s[0:1]
	v_fma_f32 v31, -v36, v31, v1
	v_cmp_lt_f32_e64 s[0:1], 0, v31
	s_nop 1
	v_cndmask_b32_e64 v31, v35, v36, s[0:1]
	v_mul_f32_e32 v35, 0x37800000, v31
	v_cndmask_b32_e32 v31, v31, v35, vcc
	v_cmp_class_f32_e32 vcc, v1, v221
	s_nop 1
	v_cndmask_b32_e32 v1, v31, v1, vcc
	v_div_scale_f32 v31, s[0:1], v1, v1, v32
	v_rcp_f32_e32 v35, v31
	s_nop 0
	v_fma_f32 v36, -v31, v35, 1.0
	v_fmac_f32_e32 v35, v36, v35
	v_div_scale_f32 v36, vcc, v32, v1, v32
	v_mul_f32_e32 v37, v36, v35
	v_fma_f32 v38, -v31, v37, v36
	v_fmac_f32_e32 v37, v38, v35
	v_fma_f32 v31, -v31, v37, v36
	v_div_fmas_f32 v31, v31, v35, v37
	v_div_fixup_f32 v36, v31, v1, v32
	v_add_u32_e32 v1, 0xa0, v30
	v_mad_i64_i32 v[38:39], s[0:1], v1, s96, v[28:29]
	v_lshl_add_u64 v[38:39], v[38:39], 0, s[72:73]
	v_pk_mul_f32 v[40:41], v[68:69], v[36:37] op_sel_hi:[1,0]
	v_lshl_add_u64 v[38:39], v[38:39], 0, s[20:21]
	v_pk_mul_f32 v[42:43], v[70:71], v[36:37] op_sel_hi:[1,0]
	v_pk_mul_f32 v[40:41], v[24:25], v[40:41]
	v_lshl_add_u64 v[38:39], v[38:39], 0, v[2:3]
	v_pk_mul_f32 v[42:43], v[26:27], v[42:43]
	v_cvt_pk_bf16_f32 v40, v40, v41
	s_nop 0
	v_cvt_pk_bf16_f32 v41, v42, v43
	global_store_dwordx2 v[38:39], v[40:41], off
	v_pk_mul_f32 v[40:41], v[64:65], v[36:37] op_sel_hi:[1,0]
	v_pk_mul_f32 v[42:43], v[66:67], v[36:37] op_sel_hi:[1,0]
	v_pk_mul_f32 v[40:41], v[20:21], v[40:41]
	v_pk_mul_f32 v[42:43], v[22:23], v[42:43]
	v_cvt_pk_bf16_f32 v40, v40, v41
	s_nop 0
	v_cvt_pk_bf16_f32 v41, v42, v43
	global_store_dwordx2 v[38:39], v[40:41], off offset:32
	v_pk_mul_f32 v[40:41], v[60:61], v[36:37] op_sel_hi:[1,0]
	v_pk_mul_f32 v[42:43], v[62:63], v[36:37] op_sel_hi:[1,0]
	v_pk_mul_f32 v[40:41], v[8:9], v[40:41]
	v_pk_mul_f32 v[42:43], v[10:11], v[42:43]
	v_cvt_pk_bf16_f32 v40, v40, v41
	s_nop 0
	v_cvt_pk_bf16_f32 v41, v42, v43
	global_store_dwordx2 v[38:39], v[40:41], off offset:64
	v_pk_mul_f32 v[40:41], v[56:57], v[36:37] op_sel_hi:[1,0]
	v_pk_mul_f32 v[36:37], v[58:59], v[36:37] op_sel_hi:[1,0]
	v_pk_mul_f32 v[40:41], v[4:5], v[40:41]
	v_pk_mul_f32 v[36:37], v[6:7], v[36:37]
	v_cvt_pk_bf16_f32 v40, v40, v41
	v_pk_mul_f32 v[58:59], v[12:13], s[74:75] op_sel_hi:[1,0]
	v_cvt_pk_bf16_f32 v41, v36, v37
	global_store_dwordx2 v[38:39], v[40:41], off offset:96
	v_pk_mul_f32 v[36:37], v[54:55], s[74:75] op_sel_hi:[1,0]
	v_pk_mul_f32 v[38:39], v[52:53], s[74:75] op_sel_hi:[1,0]
	v_pk_mul_f32 v[36:37], v[36:37], v[36:37]
	v_pk_mul_f32 v[38:39], v[38:39], v[38:39]
	v_mul_f32_e32 v1, v58, v58
	v_pk_mov_b32 v[40:41], v[38:39], v[36:37] op_sel:[1,0]
	v_mov_b32_e32 v39, v37
	v_pk_add_f32 v[36:37], v[40:41], v[38:39]
	v_pk_mul_f32 v[38:39], v[50:51], s[74:75] op_sel_hi:[1,0]
	v_pk_mul_f32 v[40:41], v[48:49], s[74:75] op_sel_hi:[1,0]
	v_pk_mul_f32 v[38:39], v[38:39], v[38:39]
	v_pk_mul_f32 v[40:41], v[40:41], v[40:41]
	v_mul_f32_e32 v31, v59, v59
	v_pk_mov_b32 v[42:43], v[40:41], v[38:39] op_sel:[1,0]
	v_mov_b32_e32 v41, v39
	v_pk_add_f32 v[38:39], v[42:43], v[40:41]
	v_pk_add_f32 v[36:37], v[36:37], v[36:37] op_sel:[0,1] op_sel_hi:[1,0]
	v_pk_add_f32 v[38:39], v[38:39], v[38:39] op_sel:[0,1] op_sel_hi:[1,0]
	v_pk_mul_f32 v[42:43], v[44:45], s[74:75] op_sel_hi:[1,0]
	v_mov_b32_e32 v37, v1
	v_mov_b32_e32 v39, v31
	v_pk_mul_f32 v[40:41], v[46:47], s[74:75] op_sel_hi:[1,0]
	v_pk_add_f32 v[36:37], v[36:37], v[38:39]
	v_mul_f32_e32 v38, v43, v43
	v_pk_mul_f32 v[56:57], v[14:15], s[74:75] op_sel_hi:[1,0]
	v_pk_fma_f32 v[38:39], v[42:43], v[42:43], v[38:39] op_sel_hi:[1,1,0]
	v_mul_f32_e32 v42, v41, v41
	v_mul_f32_e32 v35, v56, v56
	v_mul_f32_e32 v56, v57, v57
	v_pk_fma_f32 v[40:41], v[40:41], v[40:41], v[42:43] op_sel_hi:[1,1,0]
	v_mov_b32_e32 v39, v35
	v_mov_b32_e32 v41, v56
	v_pk_add_f32 v[38:39], v[38:39], v[40:41]
	s_nop 0
	v_pk_add_f32 v[36:37], v[36:37], v[38:39]
	s_nop 0
	v_add_f32_e32 v1, v36, v37
	s_waitcnt lgkmcnt(0)
	v_mov_b32_e32 v31, v1
	s_nop 1
	v_permlane16_swap_b32_e32 v31, v1
	v_add_f32_e32 v1, v1, v31
	s_waitcnt lgkmcnt(0)
	v_mov_b32_e32 v31, v1
	s_nop 1
	v_permlane32_swap_b32_e32 v31, v1
	v_add_f32_e32 v1, v1, v31
	v_fmamk_f32 v1, v1, 0x3c800000, v220
	v_cmp_gt_f32_e32 vcc, s93, v1
	v_mul_f32_e32 v31, 0x4f800000, v1
	s_nop 0
	v_cndmask_b32_e32 v1, v1, v31, vcc
	v_sqrt_f32_e32 v31, v1
	s_nop 0
	v_add_u32_e32 v33, -1, v31
	v_fma_f32 v34, -v33, v31, v1
	v_cmp_ge_f32_e64 s[0:1], 0, v34
	v_add_u32_e32 v34, 1, v31
	s_nop 0
	v_cndmask_b32_e64 v33, v31, v33, s[0:1]
	v_fma_f32 v31, -v34, v31, v1
	v_cmp_lt_f32_e64 s[0:1], 0, v31
	s_nop 1
	v_cndmask_b32_e64 v31, v33, v34, s[0:1]
	v_mul_f32_e32 v33, 0x37800000, v31
	v_cndmask_b32_e32 v31, v31, v33, vcc
	v_cmp_class_f32_e32 vcc, v1, v221
	s_nop 1
	v_cndmask_b32_e32 v1, v31, v1, vcc
	v_div_scale_f32 v31, s[0:1], v1, v1, v32
	v_rcp_f32_e32 v33, v31
	s_nop 0
	v_fma_f32 v34, -v31, v33, 1.0
	v_fmac_f32_e32 v33, v34, v33
	v_div_scale_f32 v34, vcc, v32, v1, v32
	v_mul_f32_e32 v35, v34, v33
	v_fma_f32 v36, -v31, v35, v34
	v_fmac_f32_e32 v35, v36, v33
	v_fma_f32 v31, -v31, v35, v34
	v_div_fmas_f32 v31, v31, v33, v35
	v_div_fixup_f32 v32, v31, v1, v32
	v_add_u32_e32 v1, 0xb0, v30
	v_mad_i64_i32 v[28:29], s[0:1], v1, s96, v[28:29]
	v_lshl_add_u64 v[28:29], v[28:29], 0, s[72:73]
	v_pk_mul_f32 v[30:31], v[52:53], v[32:33] op_sel_hi:[1,0]
	v_lshl_add_u64 v[28:29], v[28:29], 0, s[20:21]
	v_pk_mul_f32 v[34:35], v[54:55], v[32:33] op_sel_hi:[1,0]
	v_pk_mul_f32 v[24:25], v[24:25], v[30:31]
	v_lshl_add_u64 v[28:29], v[28:29], 0, v[2:3]
	v_pk_mul_f32 v[26:27], v[26:27], v[34:35]
	v_cvt_pk_bf16_f32 v24, v24, v25
	s_nop 0
	v_cvt_pk_bf16_f32 v25, v26, v27
	global_store_dwordx2 v[28:29], v[24:25], off
	v_pk_mul_f32 v[24:25], v[48:49], v[32:33] op_sel_hi:[1,0]
	v_pk_mul_f32 v[26:27], v[50:51], v[32:33] op_sel_hi:[1,0]
	v_pk_mul_f32 v[20:21], v[20:21], v[24:25]
	v_pk_mul_f32 v[22:23], v[22:23], v[26:27]
	v_cvt_pk_bf16_f32 v20, v20, v21
	s_nop 0
	v_cvt_pk_bf16_f32 v21, v22, v23
	global_store_dwordx2 v[28:29], v[20:21], off offset:32
	v_pk_mul_f32 v[20:21], v[44:45], v[32:33] op_sel_hi:[1,0]
	v_pk_mul_f32 v[22:23], v[46:47], v[32:33] op_sel_hi:[1,0]
	v_pk_mul_f32 v[8:9], v[8:9], v[20:21]
	v_pk_mul_f32 v[10:11], v[10:11], v[22:23]
	v_cvt_pk_bf16_f32 v8, v8, v9
	s_nop 0
	v_cvt_pk_bf16_f32 v9, v10, v11
	global_store_dwordx2 v[28:29], v[8:9], off offset:64
	v_pk_mul_f32 v[8:9], v[12:13], v[32:33] op_sel_hi:[1,0]
	v_pk_mul_f32 v[10:11], v[14:15], v[32:33] op_sel_hi:[1,0]
	v_pk_mul_f32 v[4:5], v[4:5], v[8:9]
	v_pk_mul_f32 v[6:7], v[6:7], v[10:11]
	v_cvt_pk_bf16_f32 v4, v4, v5
	s_nop 0
	v_cvt_pk_bf16_f32 v5, v6, v7
	global_store_dwordx2 v[28:29], v[4:5], off offset:96
	s_andn2_b64 vcc, exec, s[6:7]
	s_mov_b64 s[0:1], -1
	s_cbranch_vccnz .LBB0_1051

.LBB0_1216:
	s_mov_b32 s0, 4
	s_ashr_i32 s1, s0, 31
	s_lshl_b64 s[0:1], s[0:1], 3
	s_add_u32 s0, s94, s0
	s_addc_u32 s1, s95, s1
	s_load_dwordx2 s[0:1], s[0:1], 0x0
	v_mov_b32_e32 v19, v0
	v_mov_b64_e32 v[6:7], s[28:29]
	s_waitcnt lgkmcnt(0)
	s_add_u32 s12, s0, s4
	s_mov_b32 s0, 5
	s_addc_u32 s13, s1, s5
	s_ashr_i32 s1, s0, 31
	s_lshl_b64 s[0:1], s[0:1], 3
	s_add_u32 s0, s94, s0
	s_addc_u32 s1, s95, s1
	s_load_dwordx2 s[8:9], s[0:1], 0x0
	s_mov_b32 s0, 6
	s_ashr_i32 s1, s0, 31
	s_lshl_b64 s[0:1], s[0:1], 3
	s_add_u32 s0, s94, s0
	s_addc_u32 s1, s95, s1
	s_load_dwordx2 s[10:11], s[0:1], 0x0
	s_and_b32 s21, s16, 0xffffff80
	v_ashrrev_i32_e32 v5, 2, v19
	v_lshlrev_b32_e32 v1, 5, v19
	v_and_b32_e32 v4, 0x60, v1
	v_add_u32_e32 v1, s21, v5
	v_mad_i64_i32 v[6:7], s[0:1], v1, s96, v[6:7]
	s_and_b32 s72, s18, 0x180
	s_lshl_b32 s0, s72, 1
	s_mov_b32 s1, s73
	v_lshl_add_u64 v[6:7], v[6:7], 0, s[0:1]
	v_lshlrev_b32_e32 v2, 1, v4
	v_lshl_add_u64 v[14:15], v[6:7], 0, v[2:3]
	global_load_dwordx4 v[40:43], v[14:15], off offset:1072
	global_load_dwordx4 v[6:9], v[14:15], off offset:1056
	global_load_dwordx4 v[10:13], v[14:15], off offset:1040
	s_nop 0
	global_load_dwordx4 v[14:17], v[14:15], off offset:1024
	v_readfirstlane_b32 s100, v19
	s_ashr_i32 s100, s100, 2
	v_bfi_b32 v120, -16, s100, v19
	v_ashrrev_i32_e32 v121, 31, v120
	v_lshl_add_u64 v[120:121], v[120:121], 0, s[72:73]
	v_lshlrev_b64 v[120:121], 9, v[120:121]
	v_lshl_add_u64 v[120:121], s[12:13], 0, v[120:121]
	v_bfe_u32 v122, v19, 4, 2
	v_lshlrev_b32_e32 v122, 5, v122
	v_mov_b32_e32 v123, 0
	v_lshl_add_u64 v[120:121], v[120:121], 0, v[122:123]
	global_load_dwordx4 v[124:127], v[120:121], off
	global_load_dwordx4 v[128:131], v[120:121], off offset:16
	global_load_dwordx4 v[132:135], v[120:121], off offset:128
	global_load_dwordx4 v[136:139], v[120:121], off offset:144
	global_load_dwordx4 v[140:143], v[120:121], off offset:256
	global_load_dwordx4 v[144:147], v[120:121], off offset:272
	global_load_dwordx4 v[148:151], v[120:121], off offset:384
	global_load_dwordx4 v[152:155], v[120:121], off offset:400
	v_lshlrev_b32_e32 v5, 1, v5
	v_mul_u32_u24_e32 v4, 0x110, v4
	v_add3_u32 v4, 0, v4, v5
	v_bfe_u32 v47, v19, 4, 2
	v_and_b32_e32 v46, 15, v19
	v_lshlrev_b32_e32 v48, 3, v47
	v_lshlrev_b32_e32 v44, 2, v48
	s_waitcnt vmcnt(10)
	v_lshlrev_b32_e32 v24, 16, v6
	s_waitcnt vmcnt(9)
	v_and_b32_e32 v27, 0xffff0000, v10
	s_waitcnt vmcnt(8)
	v_and_b32_e32 v36, 0xffff0000, v14
	v_and_b32_e32 v33, 0xffff0000, v15
	v_lshlrev_b32_e32 v38, 16, v14
	v_mul_f32_e32 v1, v36, v36
	v_lshlrev_b32_e32 v37, 16, v15
	v_mul_f32_e32 v2, v33, v33
	v_fmac_f32_e32 v1, v38, v38
	v_fmac_f32_e32 v2, v37, v37
	v_and_b32_e32 v31, 0xffff0000, v16
	v_add_f32_e32 v1, v1, v2
	v_lshlrev_b32_e32 v35, 16, v16
	v_mul_f32_e32 v2, v31, v31
	v_fmac_f32_e32 v2, v35, v35
	v_and_b32_e32 v29, 0xffff0000, v17
	v_add_f32_e32 v1, v2, v1
	v_lshlrev_b32_e32 v34, 16, v17
	v_mul_f32_e32 v2, v29, v29
	v_fmac_f32_e32 v2, v34, v34
	v_add_f32_e32 v1, v2, v1
	v_lshlrev_b32_e32 v32, 16, v10
	v_mul_f32_e32 v2, v27, v27
	v_fmac_f32_e32 v2, v32, v32
	v_and_b32_e32 v25, 0xffff0000, v11
	v_add_f32_e32 v1, v2, v1
	v_lshlrev_b32_e32 v30, 16, v11
	v_mul_f32_e32 v2, v25, v25
	v_fmac_f32_e32 v2, v30, v30
	v_and_b32_e32 v23, 0xffff0000, v12
	v_add_f32_e32 v1, v2, v1
	v_lshlrev_b32_e32 v28, 16, v12
	v_mul_f32_e32 v2, v23, v23
	v_fmac_f32_e32 v2, v28, v28
	v_and_b32_e32 v21, 0xffff0000, v13
	v_add_f32_e32 v1, v2, v1
	v_lshlrev_b32_e32 v26, 16, v13
	v_mul_f32_e32 v2, v21, v21
	v_fmac_f32_e32 v2, v26, v26
	v_and_b32_e32 v17, 0xffff0000, v6
	v_add_f32_e32 v1, v2, v1
	v_mul_f32_e32 v2, v17, v17
	v_fmac_f32_e32 v2, v24, v24
	v_and_b32_e32 v15, 0xffff0000, v7
	v_add_f32_e32 v1, v2, v1
	v_lshlrev_b32_e32 v22, 16, v7
	v_mul_f32_e32 v2, v15, v15
	v_fmac_f32_e32 v2, v22, v22
	v_and_b32_e32 v13, 0xffff0000, v8
	v_add_f32_e32 v1, v2, v1
	v_lshlrev_b32_e32 v20, 16, v8
	v_mul_f32_e32 v2, v13, v13
	v_fmac_f32_e32 v2, v20, v20
	v_and_b32_e32 v11, 0xffff0000, v9
	v_add_f32_e32 v1, v2, v1
	v_lshlrev_b32_e32 v16, 16, v9
	v_mul_f32_e32 v2, v11, v11
	v_fmac_f32_e32 v2, v16, v16
	v_and_b32_e32 v9, 0xffff0000, v40
	v_add_f32_e32 v1, v2, v1
	v_lshlrev_b32_e32 v14, 16, v40
	v_mul_f32_e32 v2, v9, v9
	v_fmac_f32_e32 v2, v14, v14
	v_and_b32_e32 v7, 0xffff0000, v41
	v_add_f32_e32 v1, v2, v1
	v_lshlrev_b32_e32 v12, 16, v41
	v_mul_f32_e32 v2, v7, v7
	v_fmac_f32_e32 v2, v12, v12
	v_and_b32_e32 v6, 0xffff0000, v42
	v_add_f32_e32 v1, v2, v1
	v_lshlrev_b32_e32 v10, 16, v42
	v_mul_f32_e32 v2, v6, v6
	v_fmac_f32_e32 v2, v10, v10
	v_add_f32_e32 v1, v2, v1
	v_and_b32_e32 v2, 0xffff0000, v43
	v_lshlrev_b32_e32 v8, 16, v43
	v_mul_f32_e32 v39, v2, v2
	v_fmac_f32_e32 v39, v8, v8
	v_and_b32_e32 v40, 64, v222
	v_add_f32_e32 v39, v39, v1
	v_xor_b32_e32 v1, 1, v222
	v_add_u32_e32 v40, 64, v40
	v_cmp_lt_i32_e32 vcc, v1, v40
	s_nop 1
	v_cndmask_b32_e32 v1, v222, v1, vcc
	v_lshlrev_b32_e32 v1, 2, v1
	s_waitcnt lgkmcnt(0)
	s_nop 1
	v_add_f32_dpp v1, v39, v39 quad_perm:[1,0,3,2] row_mask:0xf bank_mask:0xf
	v_xor_b32_e32 v39, 2, v222
	v_cmp_lt_i32_e32 vcc, v39, v40
	s_nop 1
	v_cndmask_b32_e32 v39, v222, v39, vcc
	v_lshlrev_b32_e32 v39, 2, v39
	s_waitcnt lgkmcnt(0)
	s_nop 1
	v_add_f32_dpp v1, v1, v1 quad_perm:[2,3,0,1] row_mask:0xf bank_mask:0xf
	v_fmamk_f32 v1, v1, 0x3c000000, v220
	v_cmp_gt_f32_e32 vcc, s93, v1
	v_mul_f32_e32 v39, 0x4f800000, v1
	s_nop 0
	v_cndmask_b32_e32 v1, v1, v39, vcc
	v_sqrt_f32_e32 v39, v1
	s_nop 0
	v_add_u32_e32 v40, -1, v39
	v_fma_f32 v41, -v40, v39, v1
	v_cmp_ge_f32_e64 s[0:1], 0, v41
	v_add_u32_e32 v41, 1, v39
	s_nop 0
	v_cndmask_b32_e64 v40, v39, v40, s[0:1]
	v_fma_f32 v39, -v41, v39, v1
	v_cmp_lt_f32_e64 s[0:1], 0, v39
	s_nop 1
	v_cndmask_b32_e64 v39, v40, v41, s[0:1]
	v_mul_f32_e32 v40, 0x37800000, v39
	v_cndmask_b32_e32 v39, v39, v40, vcc
	v_cmp_class_f32_e32 vcc, v1, v221
	s_nop 1
	v_cndmask_b32_e32 v1, v39, v1, vcc
	v_div_scale_f32 v39, s[0:1], v1, v1, 1.0
	v_rcp_f32_e32 v40, v39
	v_readfirstlane_b32 s0, v19
	s_ashr_i32 s0, s0, 2
	s_cmp_lt_i32 s0, 0
	v_fma_f32 v41, -v39, v40, 1.0
	v_fmac_f32_e32 v40, v41, v40
	v_div_scale_f32 v41, vcc, 1.0, v1, 1.0
	v_mul_f32_e32 v42, v41, v40
	v_fma_f32 v43, -v39, v42, v41
	v_fmac_f32_e32 v42, v43, v40
	v_fma_f32 v39, -v39, v42, v41
	v_div_fmas_f32 v39, v39, v40, v42
	v_div_fixup_f32 v1, v39, v1, 1.0
	v_mul_f32_e32 v38, v1, v38
	v_mul_f32_e32 v5, v1, v36
	v_cvt_pk_bf16_f32 v38, v38, v3
	ds_write_b16 v4, v38
	v_cvt_pk_bf16_f32 v5, v5, v3
	ds_write_b16 v4, v5 offset:272
	v_mul_f32_e32 v5, v1, v37
	v_cvt_pk_bf16_f32 v5, v5, v3
	ds_write_b16 v4, v5 offset:544
	v_mul_f32_e32 v5, v1, v33
	v_cvt_pk_bf16_f32 v5, v5, v3
	ds_write_b16 v4, v5 offset:816
	v_mul_f32_e32 v5, v1, v35
	v_cvt_pk_bf16_f32 v5, v5, v3
	ds_write_b16 v4, v5 offset:1088
	v_mul_f32_e32 v5, v1, v31
	v_cvt_pk_bf16_f32 v5, v5, v3
	ds_write_b16 v4, v5 offset:1360
	v_mul_f32_e32 v5, v1, v34
	v_cvt_pk_bf16_f32 v5, v5, v3
	ds_write_b16 v4, v5 offset:1632
	v_mul_f32_e32 v5, v1, v29
	v_cvt_pk_bf16_f32 v5, v5, v3
	ds_write_b16 v4, v5 offset:1904
	v_mul_f32_e32 v5, v1, v32
	v_cvt_pk_bf16_f32 v5, v5, v3
	ds_write_b16 v4, v5 offset:2176
	v_mul_f32_e32 v5, v1, v27
	v_cvt_pk_bf16_f32 v5, v5, v3
	ds_write_b16 v4, v5 offset:2448
	v_mul_f32_e32 v5, v1, v30
	v_cvt_pk_bf16_f32 v5, v5, v3
	ds_write_b16 v4, v5 offset:2720
	v_mul_f32_e32 v5, v1, v25
	v_cvt_pk_bf16_f32 v5, v5, v3
	ds_write_b16 v4, v5 offset:2992
	v_mul_f32_e32 v5, v1, v28
	v_cvt_pk_bf16_f32 v5, v5, v3
	ds_write_b16 v4, v5 offset:3264
	v_mul_f32_e32 v5, v1, v23
	v_cvt_pk_bf16_f32 v5, v5, v3
	ds_write_b16 v4, v5 offset:3536
	v_mul_f32_e32 v5, v1, v26
	v_cvt_pk_bf16_f32 v5, v5, v3
	ds_write_b16 v4, v5 offset:3808
	v_mul_f32_e32 v5, v1, v21
	v_cvt_pk_bf16_f32 v5, v5, v3
	ds_write_b16 v4, v5 offset:4080
	v_mul_f32_e32 v5, v1, v24
	v_cvt_pk_bf16_f32 v5, v5, v3
	ds_write_b16 v4, v5 offset:4352
	v_mul_f32_e32 v5, v1, v17
	v_cvt_pk_bf16_f32 v5, v5, v3
	ds_write_b16 v4, v5 offset:4624
	v_mul_f32_e32 v5, v1, v22
	v_cvt_pk_bf16_f32 v5, v5, v3
	ds_write_b16 v4, v5 offset:4896
	v_mul_f32_e32 v5, v1, v15
	v_cvt_pk_bf16_f32 v5, v5, v3
	ds_write_b16 v4, v5 offset:5168
	v_mul_f32_e32 v5, v1, v20
	v_cvt_pk_bf16_f32 v5, v5, v3
	ds_write_b16 v4, v5 offset:5440
	v_mul_f32_e32 v5, v1, v13
	v_cvt_pk_bf16_f32 v5, v5, v3
	ds_write_b16 v4, v5 offset:5712
	v_mul_f32_e32 v5, v1, v16
	v_cvt_pk_bf16_f32 v5, v5, v3
	ds_write_b16 v4, v5 offset:5984
	v_mul_f32_e32 v5, v1, v11
	v_cvt_pk_bf16_f32 v5, v5, v3
	ds_write_b16 v4, v5 offset:6256
	v_mul_f32_e32 v5, v1, v14
	v_cvt_pk_bf16_f32 v5, v5, v3
	ds_write_b16 v4, v5 offset:6528
	v_mul_f32_e32 v5, v1, v9
	v_cvt_pk_bf16_f32 v5, v5, v3
	ds_write_b16 v4, v5 offset:6800
	v_mul_f32_e32 v5, v1, v12
	v_cvt_pk_bf16_f32 v5, v5, v3
	ds_write_b16 v4, v5 offset:7072
	v_mul_f32_e32 v5, v1, v7
	v_cvt_pk_bf16_f32 v5, v5, v3
	ds_write_b16 v4, v5 offset:7344
	v_mul_f32_e32 v5, v1, v10
	v_cvt_pk_bf16_f32 v5, v5, v3
	ds_write_b16 v4, v5 offset:7616
	v_mul_f32_e32 v5, v1, v6
	v_cvt_pk_bf16_f32 v5, v5, v3
	ds_write_b16 v4, v5 offset:7888
	v_mul_f32_e32 v5, v1, v8
	v_bfi_b32 v40, -16, s0, v19
	v_cvt_pk_bf16_f32 v5, v5, v3
	v_mul_f32_e32 v1, v1, v2
	v_ashrrev_i32_e32 v41, 31, v40
	ds_write_b16 v4, v5 offset:8160
	v_cvt_pk_bf16_f32 v1, v1, v3
	ds_write_b16 v4, v1 offset:8432
	v_lshl_add_u64 v[4:5], v[40:41], 0, s[72:73]
	v_lshlrev_b64 v[4:5], 9, v[4:5]
	v_lshl_add_u64 v[42:43], s[12:13], 0, v[4:5]
	v_mul_u32_u24_e32 v41, 0x110, v46
	s_waitcnt lgkmcnt(0)
	s_barrier
	s_cbranch_scc1 .LBB0_1218
	v_mov_b32_e32 v45, v3
	v_lshl_add_u64 v[8:9], v[42:43], 0, v[44:45]
	s_waitcnt vmcnt(0)
	v_mov_b64_e32 v[4:5], v[124:125]
	v_mov_b64_e32 v[6:7], v[126:127]
	s_nop 0
	v_mov_b64_e32 v[8:9], v[128:129]
	v_mov_b64_e32 v[10:11], v[130:131]
	v_cmp_le_i32_e32 vcc, v48, v40
	v_or_b32_e32 v1, 2, v48
	v_or_b32_e32 v2, 3, v48
	v_or_b32_e32 v12, 4, v48
	v_or_b32_e32 v13, 5, v48
	v_or_b32_e32 v14, 6, v48
	v_or_b32_e32 v15, 7, v48
	v_lshlrev_b32_e32 v16, 4, v47
	v_add3_u32 v45, 0, v16, v41
	s_waitcnt vmcnt(1)
	v_cndmask_b32_e32 v4, 0, v4, vcc
	v_cmp_lt_i32_e32 vcc, v48, v40
	s_nop 1
	v_cndmask_b32_e32 v5, 0, v5, vcc
	v_cmp_le_i32_e32 vcc, v1, v40
	v_cvt_pk_bf16_f32 v4, v4, v5
	s_nop 1
	v_cndmask_b32_e32 v1, 0, v6, vcc
	v_cmp_le_i32_e32 vcc, v2, v40
	s_nop 1
	v_cndmask_b32_e32 v2, 0, v7, vcc
	v_cmp_le_i32_e32 vcc, v12, v40
	v_cvt_pk_bf16_f32 v5, v1, v2
	s_waitcnt vmcnt(0)
	s_nop 0
	v_cndmask_b32_e32 v6, 0, v8, vcc
	v_cmp_le_i32_e32 vcc, v13, v40
	s_nop 1
	v_cndmask_b32_e32 v7, 0, v9, vcc
	v_cmp_le_i32_e32 vcc, v14, v40
	v_cvt_pk_bf16_f32 v6, v6, v7
	s_nop 1
	v_cndmask_b32_e32 v8, 0, v10, vcc
	v_cmp_le_i32_e32 vcc, v15, v40
	s_nop 1
	v_cndmask_b32_e32 v9, 0, v11, vcc
	v_cvt_pk_bf16_f32 v7, v8, v9
	ds_read_b128 v[8:11], v45
	ds_read_b128 v[12:15], v45 offset:4352
	s_waitcnt lgkmcnt(1)
	v_mfma_f32_16x16x32_bf16 v[36:39], v[4:7], v[8:11], 0
	s_waitcnt lgkmcnt(0)
	v_mfma_f32_16x16x32_bf16 v[32:35], v[4:7], v[12:15], 0
	ds_read_b128 v[8:11], v45 offset:8704
	ds_read_b128 v[12:15], v45 offset:13056
	s_waitcnt lgkmcnt(1)
	v_mfma_f32_16x16x32_bf16 v[28:31], v[4:7], v[8:11], 0
	s_waitcnt lgkmcnt(0)
	v_mfma_f32_16x16x32_bf16 v[24:27], v[4:7], v[12:15], 0
	ds_read_b128 v[8:11], v45 offset:17408
	ds_read_b128 v[12:15], v45 offset:21760
	s_waitcnt lgkmcnt(1)
	v_mfma_f32_16x16x32_bf16 v[20:23], v[4:7], v[8:11], 0
	ds_read_b128 v[8:11], v45 offset:26112
	ds_read_b128 v[50:53], v45 offset:30464
	s_waitcnt lgkmcnt(2)
	v_mfma_f32_16x16x32_bf16 v[14:17], v[4:7], v[12:15], 0
	s_waitcnt lgkmcnt(1)
	v_mfma_f32_16x16x32_bf16 v[10:13], v[4:7], v[8:11], 0
	s_waitcnt lgkmcnt(0)
	v_mfma_f32_16x16x32_bf16 v[6:9], v[4:7], v[50:53], 0
	s_or_b32 s1, s0, 15
	s_cmp_lt_i32 s1, 32
	s_cbranch_scc0 .LBB0_1219
	s_branch .LBB0_1220

.LBB0_1945:
	s_ashr_i32 s2, s10, 3
	s_ashr_i32 s3, s2, 31
	s_lshl_b64 s[2:3], s[2:3], 13
	s_add_u32 s2, s75, s2
	s_addc_u32 s3, s78, s3
	s_lshl_b64 s[0:1], s[0:1], 2
	s_add_u32 s0, s2, s0
	s_addc_u32 s1, s3, s1
	s_lshl_b32 s2, s24, 2
	s_add_u32 s0, s0, s2
	s_addc_u32 s1, s1, 0
	v_ashrrev_i32_e32 v31, 31, v30
	s_mov_b32 s2, 0xc0c00000
	s_lshl_b32 s0, s7, 7
	s_ashr_i32 s1, s0, 31
	s_mov_b32 s72, s6
	s_waitcnt vmcnt(12)
	v_mov_b32_dpp v4, v1 row_newbcast:4 row_mask:0xf bank_mask:0xf
	v_mov_b32_dpp v5, v1 row_newbcast:5 row_mask:0xf bank_mask:0xf
	v_mov_b32_dpp v6, v1 row_newbcast:6 row_mask:0xf bank_mask:0xf
	v_mov_b32_dpp v7, v1 row_newbcast:7 row_mask:0xf bank_mask:0xf
	v_mov_b32_dpp v8, v1 row_newbcast:0 row_mask:0xf bank_mask:0xf
	v_mov_b32_dpp v9, v1 row_newbcast:1 row_mask:0xf bank_mask:0xf
	v_mov_b32_dpp v10, v1 row_newbcast:2 row_mask:0xf bank_mask:0xf
	v_mov_b32_dpp v11, v1 row_newbcast:3 row_mask:0xf bank_mask:0xf
	v_mov_b32_dpp v22, v1 row_newbcast:12 row_mask:0xf bank_mask:0xf
	v_mov_b32_dpp v23, v1 row_newbcast:13 row_mask:0xf bank_mask:0xf
	v_mov_b32_dpp v24, v1 row_newbcast:14 row_mask:0xf bank_mask:0xf
	v_mov_b32_dpp v25, v1 row_newbcast:15 row_mask:0xf bank_mask:0xf
	v_mov_b32_dpp v32, v1 row_newbcast:8 row_mask:0xf bank_mask:0xf
	v_mov_b32_dpp v33, v1 row_newbcast:9 row_mask:0xf bank_mask:0xf
	v_mov_b32_dpp v34, v1 row_newbcast:10 row_mask:0xf bank_mask:0xf
	v_mov_b32_dpp v35, v1 row_newbcast:11 row_mask:0xf bank_mask:0xf
	v_pk_add_f32 v[20:21], v[24:25], 1.0 op_sel_hi:[1,0]
	v_pk_add_f32 v[26:27], v[34:35], 1.0 op_sel_hi:[1,0]
	v_pk_add_f32 v[32:33], v[32:33], 1.0 op_sel_hi:[1,0]
	v_pk_add_f32 v[22:23], v[22:23], 1.0 op_sel_hi:[1,0]
	v_lshlrev_b64 v[24:25], 10, v[30:31]
	v_lshl_add_u64 v[24:25], s[14:15], 0, v[24:25]
	v_lshl_add_u64 v[24:25], v[24:25], 0, s[0:1]
	v_lshl_add_u64 v[24:25], v[24:25], 0, s[24:25]
	v_lshl_add_u64 v[56:57], v[24:25], 0, v[28:29]
	s_mov_b32 s100, 0x3c800000
	s_mov_b32 s101, 0xc01d265f
	s_mov_b64 s[0:1], 0x4000
	v_pk_fma_f32 v[34:35], v[196:197], s[100:101], v[8:9] op_sel_hi:[1,0,1]
	v_pk_fma_f32 v[36:37], v[198:199], s[100:101], v[10:11] op_sel_hi:[1,0,1]
	v_min_f32_e32 v34, 0x40e00000, v34
	v_min_f32_e32 v35, 0x40e00000, v35
	v_min_f32_e32 v36, 0x40e00000, v36
	v_min_f32_e32 v37, 0x40e00000, v37
	v_pk_mul_f32 v[38:39], v[34:35], s[100:101] op_sel:[0,1] op_sel_hi:[1,1]
	v_pk_mul_f32 v[40:41], v[36:37], s[100:101] op_sel:[0,1] op_sel_hi:[1,1]
	v_exp_f32_e32 v38, v38
	v_exp_f32_e32 v39, v39
	v_exp_f32_e32 v40, v40
	v_exp_f32_e32 v41, v41
	v_pk_fma_f32 v[42:43], v[164:165], s[100:101], v[32:33] op_sel_hi:[1,0,1]
	v_pk_fma_f32 v[44:45], v[166:167], s[100:101], v[26:27] op_sel_hi:[1,0,1]
	v_pk_add_f32 v[38:39], v[38:39], 1.0 op_sel_hi:[1,0]
	v_pk_add_f32 v[40:41], v[40:41], 1.0 op_sel_hi:[1,0]
	v_rcp_f32_e32 v38, v38
	v_rcp_f32_e32 v39, v39
	v_rcp_f32_e32 v40, v40
	v_rcp_f32_e32 v41, v41
	v_med3_f32 v42, v42, s2, v250
	v_med3_f32 v43, v43, s2, v250
	v_med3_f32 v44, v44, s2, v250
	v_med3_f32 v45, v45, s2, v250
	v_pk_mul_f32 v[34:35], v[34:35], v[38:39]
	v_pk_mul_f32 v[36:37], v[36:37], v[40:41]
	v_pk_mul_f32 v[48:49], v[42:43], v[34:35]
	v_pk_mul_f32 v[50:51], v[44:45], v[36:37]
	v_pk_fma_f32 v[34:35], v[192:193], s[100:101], v[4:5] op_sel_hi:[1,0,1]
	v_pk_fma_f32 v[36:37], v[194:195], s[100:101], v[6:7] op_sel_hi:[1,0,1]
	v_min_f32_e32 v34, 0x40e00000, v34
	v_min_f32_e32 v35, 0x40e00000, v35
	v_min_f32_e32 v36, 0x40e00000, v36
	v_min_f32_e32 v37, 0x40e00000, v37
	v_pk_mul_f32 v[38:39], v[34:35], s[100:101] op_sel:[0,1] op_sel_hi:[1,1]
	v_pk_mul_f32 v[40:41], v[36:37], s[100:101] op_sel:[0,1] op_sel_hi:[1,1]
	v_exp_f32_e32 v38, v38
	v_exp_f32_e32 v39, v39
	v_exp_f32_e32 v40, v40
	v_exp_f32_e32 v41, v41
	v_pk_fma_f32 v[42:43], v[160:161], s[100:101], v[22:23] op_sel_hi:[1,0,1]
	v_pk_fma_f32 v[44:45], v[162:163], s[100:101], v[20:21] op_sel_hi:[1,0,1]
	v_pk_add_f32 v[38:39], v[38:39], 1.0 op_sel_hi:[1,0]
	v_pk_add_f32 v[40:41], v[40:41], 1.0 op_sel_hi:[1,0]
	v_rcp_f32_e32 v38, v38
	v_rcp_f32_e32 v39, v39
	v_rcp_f32_e32 v40, v40
	v_rcp_f32_e32 v41, v41
	v_med3_f32 v42, v42, s2, v250
	v_med3_f32 v43, v43, s2, v250
	v_med3_f32 v44, v44, s2, v250
	v_med3_f32 v45, v45, s2, v250
	v_pk_mul_f32 v[34:35], v[34:35], v[38:39]
	v_pk_mul_f32 v[36:37], v[36:37], v[40:41]
	v_pk_mul_f32 v[52:53], v[42:43], v[34:35]
	v_pk_mul_f32 v[54:55], v[44:45], v[36:37]
	v_cvt_pk_fp8_f32 v46, v48, v49
	v_cvt_pk_fp8_f32 v46, v50, v51 op_sel:[0,0,1]
	v_cvt_pk_fp8_f32 v47, v52, v53
	v_cvt_pk_fp8_f32 v47, v54, v55 op_sel:[0,0,1]
	global_store_dwordx2 v[56:57], v[46:47], off sc1
	v_lshl_add_u64 v[56:57], v[56:57], 0, s[0:1]
	v_pk_fma_f32 v[34:35], v[188:189], s[100:101], v[8:9] op_sel_hi:[1,0,1]
	v_pk_fma_f32 v[36:37], v[190:191], s[100:101], v[10:11] op_sel_hi:[1,0,1]
	v_min_f32_e32 v34, 0x40e00000, v34
	v_min_f32_e32 v35, 0x40e00000, v35
	v_min_f32_e32 v36, 0x40e00000, v36
	v_min_f32_e32 v37, 0x40e00000, v37
	v_pk_mul_f32 v[38:39], v[34:35], s[100:101] op_sel:[0,1] op_sel_hi:[1,1]
	v_pk_mul_f32 v[40:41], v[36:37], s[100:101] op_sel:[0,1] op_sel_hi:[1,1]
	v_exp_f32_e32 v38, v38
	v_exp_f32_e32 v39, v39
	v_exp_f32_e32 v40, v40
	v_exp_f32_e32 v41, v41
	v_pk_fma_f32 v[42:43], v[156:157], s[100:101], v[32:33] op_sel_hi:[1,0,1]
	v_pk_fma_f32 v[44:45], v[158:159], s[100:101], v[26:27] op_sel_hi:[1,0,1]
	v_pk_add_f32 v[38:39], v[38:39], 1.0 op_sel_hi:[1,0]
	v_pk_add_f32 v[40:41], v[40:41], 1.0 op_sel_hi:[1,0]
	v_rcp_f32_e32 v38, v38
	v_rcp_f32_e32 v39, v39
	v_rcp_f32_e32 v40, v40
	v_rcp_f32_e32 v41, v41
	v_med3_f32 v42, v42, s2, v250
	v_med3_f32 v43, v43, s2, v250
	v_med3_f32 v44, v44, s2, v250
	v_med3_f32 v45, v45, s2, v250
	v_pk_mul_f32 v[34:35], v[34:35], v[38:39]
	v_pk_mul_f32 v[36:37], v[36:37], v[40:41]
	v_pk_mul_f32 v[48:49], v[42:43], v[34:35]
	v_pk_mul_f32 v[50:51], v[44:45], v[36:37]
	v_pk_fma_f32 v[34:35], v[184:185], s[100:101], v[4:5] op_sel_hi:[1,0,1]
	v_pk_fma_f32 v[36:37], v[186:187], s[100:101], v[6:7] op_sel_hi:[1,0,1]
	v_min_f32_e32 v34, 0x40e00000, v34
	v_min_f32_e32 v35, 0x40e00000, v35
	v_min_f32_e32 v36, 0x40e00000, v36
	v_min_f32_e32 v37, 0x40e00000, v37
	v_pk_mul_f32 v[38:39], v[34:35], s[100:101] op_sel:[0,1] op_sel_hi:[1,1]
	v_pk_mul_f32 v[40:41], v[36:37], s[100:101] op_sel:[0,1] op_sel_hi:[1,1]
	v_exp_f32_e32 v38, v38
	v_exp_f32_e32 v39, v39
	v_exp_f32_e32 v40, v40
	v_exp_f32_e32 v41, v41
	v_pk_fma_f32 v[42:43], v[152:153], s[100:101], v[22:23] op_sel_hi:[1,0,1]
	v_pk_fma_f32 v[44:45], v[154:155], s[100:101], v[20:21] op_sel_hi:[1,0,1]
	v_pk_add_f32 v[38:39], v[38:39], 1.0 op_sel_hi:[1,0]
	v_pk_add_f32 v[40:41], v[40:41], 1.0 op_sel_hi:[1,0]
	v_rcp_f32_e32 v38, v38
	v_rcp_f32_e32 v39, v39
	v_rcp_f32_e32 v40, v40
	v_rcp_f32_e32 v41, v41
	v_med3_f32 v42, v42, s2, v250
	v_med3_f32 v43, v43, s2, v250
	v_med3_f32 v44, v44, s2, v250
	v_med3_f32 v45, v45, s2, v250
	v_pk_mul_f32 v[34:35], v[34:35], v[38:39]
	v_pk_mul_f32 v[36:37], v[36:37], v[40:41]
	v_pk_mul_f32 v[52:53], v[42:43], v[34:35]
	v_pk_mul_f32 v[54:55], v[44:45], v[36:37]
	v_cvt_pk_fp8_f32 v58, v48, v49
	v_cvt_pk_fp8_f32 v58, v50, v51 op_sel:[0,0,1]
	v_cvt_pk_fp8_f32 v59, v52, v53
	v_cvt_pk_fp8_f32 v59, v54, v55 op_sel:[0,0,1]
	global_store_dwordx2 v[56:57], v[58:59], off sc1
	v_lshl_add_u64 v[56:57], v[56:57], 0, s[0:1]
	v_pk_fma_f32 v[34:35], v[180:181], s[100:101], v[8:9] op_sel_hi:[1,0,1]
	v_pk_fma_f32 v[36:37], v[182:183], s[100:101], v[10:11] op_sel_hi:[1,0,1]
	v_min_f32_e32 v34, 0x40e00000, v34
	v_min_f32_e32 v35, 0x40e00000, v35
	v_min_f32_e32 v36, 0x40e00000, v36
	v_min_f32_e32 v37, 0x40e00000, v37
	v_pk_mul_f32 v[38:39], v[34:35], s[100:101] op_sel:[0,1] op_sel_hi:[1,1]
	v_pk_mul_f32 v[40:41], v[36:37], s[100:101] op_sel:[0,1] op_sel_hi:[1,1]
	v_exp_f32_e32 v38, v38
	v_exp_f32_e32 v39, v39
	v_exp_f32_e32 v40, v40
	v_exp_f32_e32 v41, v41
	v_pk_fma_f32 v[42:43], v[148:149], s[100:101], v[32:33] op_sel_hi:[1,0,1]
	v_pk_fma_f32 v[44:45], v[150:151], s[100:101], v[26:27] op_sel_hi:[1,0,1]
	v_pk_add_f32 v[38:39], v[38:39], 1.0 op_sel_hi:[1,0]
	v_pk_add_f32 v[40:41], v[40:41], 1.0 op_sel_hi:[1,0]
	v_rcp_f32_e32 v38, v38
	v_rcp_f32_e32 v39, v39
	v_rcp_f32_e32 v40, v40
	v_rcp_f32_e32 v41, v41
	v_med3_f32 v42, v42, s2, v250
	v_med3_f32 v43, v43, s2, v250
	v_med3_f32 v44, v44, s2, v250
	v_med3_f32 v45, v45, s2, v250
	v_pk_mul_f32 v[34:35], v[34:35], v[38:39]
	v_pk_mul_f32 v[36:37], v[36:37], v[40:41]
	v_pk_mul_f32 v[48:49], v[42:43], v[34:35]
	v_pk_mul_f32 v[50:51], v[44:45], v[36:37]
	v_pk_fma_f32 v[34:35], v[176:177], s[100:101], v[4:5] op_sel_hi:[1,0,1]
	v_pk_fma_f32 v[36:37], v[178:179], s[100:101], v[6:7] op_sel_hi:[1,0,1]
	v_min_f32_e32 v34, 0x40e00000, v34
	v_min_f32_e32 v35, 0x40e00000, v35
	v_min_f32_e32 v36, 0x40e00000, v36
	v_min_f32_e32 v37, 0x40e00000, v37
	v_pk_mul_f32 v[38:39], v[34:35], s[100:101] op_sel:[0,1] op_sel_hi:[1,1]
	v_pk_mul_f32 v[40:41], v[36:37], s[100:101] op_sel:[0,1] op_sel_hi:[1,1]
	v_exp_f32_e32 v38, v38
	v_exp_f32_e32 v39, v39
	v_exp_f32_e32 v40, v40
	v_exp_f32_e32 v41, v41
	v_pk_fma_f32 v[42:43], v[144:145], s[100:101], v[22:23] op_sel_hi:[1,0,1]
	v_pk_fma_f32 v[44:45], v[146:147], s[100:101], v[20:21] op_sel_hi:[1,0,1]
	v_pk_add_f32 v[38:39], v[38:39], 1.0 op_sel_hi:[1,0]
	v_pk_add_f32 v[40:41], v[40:41], 1.0 op_sel_hi:[1,0]
	v_rcp_f32_e32 v38, v38
	v_rcp_f32_e32 v39, v39
	v_rcp_f32_e32 v40, v40
	v_rcp_f32_e32 v41, v41
	v_med3_f32 v42, v42, s2, v250
	v_med3_f32 v43, v43, s2, v250
	v_med3_f32 v44, v44, s2, v250
	v_med3_f32 v45, v45, s2, v250
	v_pk_mul_f32 v[34:35], v[34:35], v[38:39]
	v_pk_mul_f32 v[36:37], v[36:37], v[40:41]
	v_pk_mul_f32 v[52:53], v[42:43], v[34:35]
	v_pk_mul_f32 v[54:55], v[44:45], v[36:37]
	v_cvt_pk_fp8_f32 v46, v48, v49
	v_cvt_pk_fp8_f32 v46, v50, v51 op_sel:[0,0,1]
	v_cvt_pk_fp8_f32 v47, v52, v53
	v_cvt_pk_fp8_f32 v47, v54, v55 op_sel:[0,0,1]
	global_store_dwordx2 v[56:57], v[46:47], off sc1
	v_lshl_add_u64 v[56:57], v[56:57], 0, s[0:1]
	v_pk_fma_f32 v[34:35], v[172:173], s[100:101], v[8:9] op_sel_hi:[1,0,1]
	v_pk_fma_f32 v[36:37], v[174:175], s[100:101], v[10:11] op_sel_hi:[1,0,1]
	v_min_f32_e32 v34, 0x40e00000, v34
	v_min_f32_e32 v35, 0x40e00000, v35
	v_min_f32_e32 v36, 0x40e00000, v36
	v_min_f32_e32 v37, 0x40e00000, v37
	v_pk_mul_f32 v[38:39], v[34:35], s[100:101] op_sel:[0,1] op_sel_hi:[1,1]
	v_pk_mul_f32 v[40:41], v[36:37], s[100:101] op_sel:[0,1] op_sel_hi:[1,1]
	v_exp_f32_e32 v38, v38
	v_exp_f32_e32 v39, v39
	v_exp_f32_e32 v40, v40
	v_exp_f32_e32 v41, v41
	v_pk_fma_f32 v[42:43], v[140:141], s[100:101], v[32:33] op_sel_hi:[1,0,1]
	v_pk_fma_f32 v[44:45], v[142:143], s[100:101], v[26:27] op_sel_hi:[1,0,1]
	v_pk_add_f32 v[38:39], v[38:39], 1.0 op_sel_hi:[1,0]
	v_pk_add_f32 v[40:41], v[40:41], 1.0 op_sel_hi:[1,0]
	v_rcp_f32_e32 v38, v38
	v_rcp_f32_e32 v39, v39
	v_rcp_f32_e32 v40, v40
	v_rcp_f32_e32 v41, v41
	v_med3_f32 v42, v42, s2, v250
	v_med3_f32 v43, v43, s2, v250
	v_med3_f32 v44, v44, s2, v250
	v_med3_f32 v45, v45, s2, v250
	v_pk_mul_f32 v[34:35], v[34:35], v[38:39]
	v_pk_mul_f32 v[36:37], v[36:37], v[40:41]
	v_pk_mul_f32 v[48:49], v[42:43], v[34:35]
	v_pk_mul_f32 v[50:51], v[44:45], v[36:37]
	v_pk_fma_f32 v[34:35], v[168:169], s[100:101], v[4:5] op_sel_hi:[1,0,1]
	v_pk_fma_f32 v[36:37], v[170:171], s[100:101], v[6:7] op_sel_hi:[1,0,1]
	v_min_f32_e32 v34, 0x40e00000, v34
	v_min_f32_e32 v35, 0x40e00000, v35
	v_min_f32_e32 v36, 0x40e00000, v36
	v_min_f32_e32 v37, 0x40e00000, v37
	v_pk_mul_f32 v[38:39], v[34:35], s[100:101] op_sel:[0,1] op_sel_hi:[1,1]
	v_pk_mul_f32 v[40:41], v[36:37], s[100:101] op_sel:[0,1] op_sel_hi:[1,1]
	v_exp_f32_e32 v38, v38
	v_exp_f32_e32 v39, v39
	v_exp_f32_e32 v40, v40
	v_exp_f32_e32 v41, v41
	v_pk_fma_f32 v[42:43], v[136:137], s[100:101], v[22:23] op_sel_hi:[1,0,1]
	v_pk_fma_f32 v[44:45], v[138:139], s[100:101], v[20:21] op_sel_hi:[1,0,1]
	v_pk_add_f32 v[38:39], v[38:39], 1.0 op_sel_hi:[1,0]
	v_pk_add_f32 v[40:41], v[40:41], 1.0 op_sel_hi:[1,0]
	v_rcp_f32_e32 v38, v38
	v_rcp_f32_e32 v39, v39
	v_rcp_f32_e32 v40, v40
	v_rcp_f32_e32 v41, v41
	v_med3_f32 v42, v42, s2, v250
	v_med3_f32 v43, v43, s2, v250
	v_med3_f32 v44, v44, s2, v250
	v_med3_f32 v45, v45, s2, v250
	v_pk_mul_f32 v[34:35], v[34:35], v[38:39]
	v_pk_mul_f32 v[36:37], v[36:37], v[40:41]
	v_pk_mul_f32 v[52:53], v[42:43], v[34:35]
	v_pk_mul_f32 v[54:55], v[44:45], v[36:37]
	v_cvt_pk_fp8_f32 v58, v48, v49
	v_cvt_pk_fp8_f32 v58, v50, v51 op_sel:[0,0,1]
	v_cvt_pk_fp8_f32 v59, v52, v53
	v_cvt_pk_fp8_f32 v59, v54, v55 op_sel:[0,0,1]
	global_store_dwordx2 v[56:57], v[58:59], off sc1
	v_lshl_add_u64 v[56:57], v[56:57], 0, s[0:1]
	v_lshl_add_u64 v[56:57], v[56:57], 0, s[0:1]
	v_lshl_add_u64 v[56:57], v[56:57], 0, s[0:1]
	v_lshl_add_u64 v[56:57], v[56:57], 0, s[0:1]
	v_lshl_add_u64 v[56:57], v[56:57], 0, s[0:1]
	v_pk_fma_f32 v[34:35], v[132:133], s[100:101], v[8:9] op_sel_hi:[1,0,1]
	v_pk_fma_f32 v[36:37], v[134:135], s[100:101], v[10:11] op_sel_hi:[1,0,1]
	v_min_f32_e32 v34, 0x40e00000, v34
	v_min_f32_e32 v35, 0x40e00000, v35
	v_min_f32_e32 v36, 0x40e00000, v36
	v_min_f32_e32 v37, 0x40e00000, v37
	v_pk_mul_f32 v[38:39], v[34:35], s[100:101] op_sel:[0,1] op_sel_hi:[1,1]
	v_pk_mul_f32 v[40:41], v[36:37], s[100:101] op_sel:[0,1] op_sel_hi:[1,1]
	v_exp_f32_e32 v38, v38
	v_exp_f32_e32 v39, v39
	v_exp_f32_e32 v40, v40
	v_exp_f32_e32 v41, v41
	v_pk_fma_f32 v[42:43], v[100:101], s[100:101], v[32:33] op_sel_hi:[1,0,1]
	v_pk_fma_f32 v[44:45], v[102:103], s[100:101], v[26:27] op_sel_hi:[1,0,1]
	v_pk_add_f32 v[38:39], v[38:39], 1.0 op_sel_hi:[1,0]
	v_pk_add_f32 v[40:41], v[40:41], 1.0 op_sel_hi:[1,0]
	v_rcp_f32_e32 v38, v38
	v_rcp_f32_e32 v39, v39
	v_rcp_f32_e32 v40, v40
	v_rcp_f32_e32 v41, v41
	v_med3_f32 v42, v42, s2, v250
	v_med3_f32 v43, v43, s2, v250
	v_med3_f32 v44, v44, s2, v250
	v_med3_f32 v45, v45, s2, v250
	v_pk_mul_f32 v[34:35], v[34:35], v[38:39]
	v_pk_mul_f32 v[36:37], v[36:37], v[40:41]
	v_pk_mul_f32 v[48:49], v[42:43], v[34:35]
	v_pk_mul_f32 v[50:51], v[44:45], v[36:37]
	v_pk_fma_f32 v[34:35], v[128:129], s[100:101], v[4:5] op_sel_hi:[1,0,1]
	v_pk_fma_f32 v[36:37], v[130:131], s[100:101], v[6:7] op_sel_hi:[1,0,1]
	v_min_f32_e32 v34, 0x40e00000, v34
	v_min_f32_e32 v35, 0x40e00000, v35
	v_min_f32_e32 v36, 0x40e00000, v36
	v_min_f32_e32 v37, 0x40e00000, v37
	v_pk_mul_f32 v[38:39], v[34:35], s[100:101] op_sel:[0,1] op_sel_hi:[1,1]
	v_pk_mul_f32 v[40:41], v[36:37], s[100:101] op_sel:[0,1] op_sel_hi:[1,1]
	v_exp_f32_e32 v38, v38
	v_exp_f32_e32 v39, v39
	v_exp_f32_e32 v40, v40
	v_exp_f32_e32 v41, v41
	v_pk_fma_f32 v[42:43], v[96:97], s[100:101], v[22:23] op_sel_hi:[1,0,1]
	v_pk_fma_f32 v[44:45], v[98:99], s[100:101], v[20:21] op_sel_hi:[1,0,1]
	v_pk_add_f32 v[38:39], v[38:39], 1.0 op_sel_hi:[1,0]
	v_pk_add_f32 v[40:41], v[40:41], 1.0 op_sel_hi:[1,0]
	v_rcp_f32_e32 v38, v38
	v_rcp_f32_e32 v39, v39
	v_rcp_f32_e32 v40, v40
	v_rcp_f32_e32 v41, v41
	v_med3_f32 v42, v42, s2, v250
	v_med3_f32 v43, v43, s2, v250
	v_med3_f32 v44, v44, s2, v250
	v_med3_f32 v45, v45, s2, v250
	v_pk_mul_f32 v[34:35], v[34:35], v[38:39]
	v_pk_mul_f32 v[36:37], v[36:37], v[40:41]
	v_pk_mul_f32 v[52:53], v[42:43], v[34:35]
	v_pk_mul_f32 v[54:55], v[44:45], v[36:37]
	v_cvt_pk_fp8_f32 v46, v48, v49
	v_cvt_pk_fp8_f32 v46, v50, v51 op_sel:[0,0,1]
	v_cvt_pk_fp8_f32 v47, v52, v53
	v_cvt_pk_fp8_f32 v47, v54, v55 op_sel:[0,0,1]
	global_store_dwordx2 v[56:57], v[46:47], off sc1
	v_lshl_add_u64 v[56:57], v[56:57], 0, s[0:1]
	v_pk_fma_f32 v[34:35], v[124:125], s[100:101], v[8:9] op_sel_hi:[1,0,1]
	v_pk_fma_f32 v[36:37], v[126:127], s[100:101], v[10:11] op_sel_hi:[1,0,1]
	v_min_f32_e32 v34, 0x40e00000, v34
	v_min_f32_e32 v35, 0x40e00000, v35
	v_min_f32_e32 v36, 0x40e00000, v36
	v_min_f32_e32 v37, 0x40e00000, v37
	v_pk_mul_f32 v[38:39], v[34:35], s[100:101] op_sel:[0,1] op_sel_hi:[1,1]
	v_pk_mul_f32 v[40:41], v[36:37], s[100:101] op_sel:[0,1] op_sel_hi:[1,1]
	v_exp_f32_e32 v38, v38
	v_exp_f32_e32 v39, v39
	v_exp_f32_e32 v40, v40
	v_exp_f32_e32 v41, v41
	v_pk_fma_f32 v[42:43], v[92:93], s[100:101], v[32:33] op_sel_hi:[1,0,1]
	v_pk_fma_f32 v[44:45], v[94:95], s[100:101], v[26:27] op_sel_hi:[1,0,1]
	v_pk_add_f32 v[38:39], v[38:39], 1.0 op_sel_hi:[1,0]
	v_pk_add_f32 v[40:41], v[40:41], 1.0 op_sel_hi:[1,0]
	v_rcp_f32_e32 v38, v38
	v_rcp_f32_e32 v39, v39
	v_rcp_f32_e32 v40, v40
	v_rcp_f32_e32 v41, v41
	v_med3_f32 v42, v42, s2, v250
	v_med3_f32 v43, v43, s2, v250
	v_med3_f32 v44, v44, s2, v250
	v_med3_f32 v45, v45, s2, v250
	v_pk_mul_f32 v[34:35], v[34:35], v[38:39]
	v_pk_mul_f32 v[36:37], v[36:37], v[40:41]
	v_pk_mul_f32 v[48:49], v[42:43], v[34:35]
	v_pk_mul_f32 v[50:51], v[44:45], v[36:37]
	v_pk_fma_f32 v[34:35], v[120:121], s[100:101], v[4:5] op_sel_hi:[1,0,1]
	v_pk_fma_f32 v[36:37], v[122:123], s[100:101], v[6:7] op_sel_hi:[1,0,1]
	v_min_f32_e32 v34, 0x40e00000, v34
	v_min_f32_e32 v35, 0x40e00000, v35
	v_min_f32_e32 v36, 0x40e00000, v36
	v_min_f32_e32 v37, 0x40e00000, v37
	v_pk_mul_f32 v[38:39], v[34:35], s[100:101] op_sel:[0,1] op_sel_hi:[1,1]
	v_pk_mul_f32 v[40:41], v[36:37], s[100:101] op_sel:[0,1] op_sel_hi:[1,1]
	v_exp_f32_e32 v38, v38
	v_exp_f32_e32 v39, v39
	v_exp_f32_e32 v40, v40
	v_exp_f32_e32 v41, v41
	v_pk_fma_f32 v[42:43], v[88:89], s[100:101], v[22:23] op_sel_hi:[1,0,1]
	v_pk_fma_f32 v[44:45], v[90:91], s[100:101], v[20:21] op_sel_hi:[1,0,1]
	v_pk_add_f32 v[38:39], v[38:39], 1.0 op_sel_hi:[1,0]
	v_pk_add_f32 v[40:41], v[40:41], 1.0 op_sel_hi:[1,0]
	v_rcp_f32_e32 v38, v38
	v_rcp_f32_e32 v39, v39
	v_rcp_f32_e32 v40, v40
	v_rcp_f32_e32 v41, v41
	v_med3_f32 v42, v42, s2, v250
	v_med3_f32 v43, v43, s2, v250
	v_med3_f32 v44, v44, s2, v250
	v_med3_f32 v45, v45, s2, v250
	v_pk_mul_f32 v[34:35], v[34:35], v[38:39]
	v_pk_mul_f32 v[36:37], v[36:37], v[40:41]
	v_pk_mul_f32 v[52:53], v[42:43], v[34:35]
	v_pk_mul_f32 v[54:55], v[44:45], v[36:37]
	v_cvt_pk_fp8_f32 v58, v48, v49
	v_cvt_pk_fp8_f32 v58, v50, v51 op_sel:[0,0,1]
	v_cvt_pk_fp8_f32 v59, v52, v53
	v_cvt_pk_fp8_f32 v59, v54, v55 op_sel:[0,0,1]
	global_store_dwordx2 v[56:57], v[58:59], off sc1
	v_lshl_add_u64 v[56:57], v[56:57], 0, s[0:1]
	v_pk_fma_f32 v[34:35], v[116:117], s[100:101], v[8:9] op_sel_hi:[1,0,1]
	v_pk_fma_f32 v[36:37], v[118:119], s[100:101], v[10:11] op_sel_hi:[1,0,1]
	v_min_f32_e32 v34, 0x40e00000, v34
	v_min_f32_e32 v35, 0x40e00000, v35
	v_min_f32_e32 v36, 0x40e00000, v36
	v_min_f32_e32 v37, 0x40e00000, v37
	v_pk_mul_f32 v[38:39], v[34:35], s[100:101] op_sel:[0,1] op_sel_hi:[1,1]
	v_pk_mul_f32 v[40:41], v[36:37], s[100:101] op_sel:[0,1] op_sel_hi:[1,1]
	v_exp_f32_e32 v38, v38
	v_exp_f32_e32 v39, v39
	v_exp_f32_e32 v40, v40
	v_exp_f32_e32 v41, v41
	v_pk_fma_f32 v[42:43], v[84:85], s[100:101], v[32:33] op_sel_hi:[1,0,1]
	v_pk_fma_f32 v[44:45], v[86:87], s[100:101], v[26:27] op_sel_hi:[1,0,1]
	v_pk_add_f32 v[38:39], v[38:39], 1.0 op_sel_hi:[1,0]
	v_pk_add_f32 v[40:41], v[40:41], 1.0 op_sel_hi:[1,0]
	v_rcp_f32_e32 v38, v38
	v_rcp_f32_e32 v39, v39
	v_rcp_f32_e32 v40, v40
	v_rcp_f32_e32 v41, v41
	v_med3_f32 v42, v42, s2, v250
	v_med3_f32 v43, v43, s2, v250
	v_med3_f32 v44, v44, s2, v250
	v_med3_f32 v45, v45, s2, v250
	v_pk_mul_f32 v[34:35], v[34:35], v[38:39]
	v_pk_mul_f32 v[36:37], v[36:37], v[40:41]
	v_pk_mul_f32 v[48:49], v[42:43], v[34:35]
	v_pk_mul_f32 v[50:51], v[44:45], v[36:37]
	v_pk_fma_f32 v[34:35], v[112:113], s[100:101], v[4:5] op_sel_hi:[1,0,1]
	v_pk_fma_f32 v[36:37], v[114:115], s[100:101], v[6:7] op_sel_hi:[1,0,1]
	v_min_f32_e32 v34, 0x40e00000, v34
	v_min_f32_e32 v35, 0x40e00000, v35
	v_min_f32_e32 v36, 0x40e00000, v36
	v_min_f32_e32 v37, 0x40e00000, v37
	v_pk_mul_f32 v[38:39], v[34:35], s[100:101] op_sel:[0,1] op_sel_hi:[1,1]
	v_pk_mul_f32 v[40:41], v[36:37], s[100:101] op_sel:[0,1] op_sel_hi:[1,1]
	v_exp_f32_e32 v38, v38
	v_exp_f32_e32 v39, v39
	v_exp_f32_e32 v40, v40
	v_exp_f32_e32 v41, v41
	v_pk_fma_f32 v[42:43], v[80:81], s[100:101], v[22:23] op_sel_hi:[1,0,1]
	v_pk_fma_f32 v[44:45], v[82:83], s[100:101], v[20:21] op_sel_hi:[1,0,1]
	v_pk_add_f32 v[38:39], v[38:39], 1.0 op_sel_hi:[1,0]
	v_pk_add_f32 v[40:41], v[40:41], 1.0 op_sel_hi:[1,0]
	v_rcp_f32_e32 v38, v38
	v_rcp_f32_e32 v39, v39
	v_rcp_f32_e32 v40, v40
	v_rcp_f32_e32 v41, v41
	v_med3_f32 v42, v42, s2, v250
	v_med3_f32 v43, v43, s2, v250
	v_med3_f32 v44, v44, s2, v250
	v_med3_f32 v45, v45, s2, v250
	v_pk_mul_f32 v[34:35], v[34:35], v[38:39]
	v_pk_mul_f32 v[36:37], v[36:37], v[40:41]
	v_pk_mul_f32 v[52:53], v[42:43], v[34:35]
	v_pk_mul_f32 v[54:55], v[44:45], v[36:37]
	v_cvt_pk_fp8_f32 v46, v48, v49
	v_cvt_pk_fp8_f32 v46, v50, v51 op_sel:[0,0,1]
	v_cvt_pk_fp8_f32 v47, v52, v53
	v_cvt_pk_fp8_f32 v47, v54, v55 op_sel:[0,0,1]
	global_store_dwordx2 v[56:57], v[46:47], off sc1
	v_lshl_add_u64 v[56:57], v[56:57], 0, s[0:1]
	v_pk_fma_f32 v[34:35], v[108:109], s[100:101], v[8:9] op_sel_hi:[1,0,1]
	v_pk_fma_f32 v[36:37], v[110:111], s[100:101], v[10:11] op_sel_hi:[1,0,1]
	v_min_f32_e32 v34, 0x40e00000, v34
	v_min_f32_e32 v35, 0x40e00000, v35
	v_min_f32_e32 v36, 0x40e00000, v36
	v_min_f32_e32 v37, 0x40e00000, v37
	v_pk_mul_f32 v[38:39], v[34:35], s[100:101] op_sel:[0,1] op_sel_hi:[1,1]
	v_pk_mul_f32 v[40:41], v[36:37], s[100:101] op_sel:[0,1] op_sel_hi:[1,1]
	v_exp_f32_e32 v38, v38
	v_exp_f32_e32 v39, v39
	v_exp_f32_e32 v40, v40
	v_exp_f32_e32 v41, v41
	v_pk_fma_f32 v[42:43], v[76:77], s[100:101], v[32:33] op_sel_hi:[1,0,1]
	v_pk_fma_f32 v[44:45], v[78:79], s[100:101], v[26:27] op_sel_hi:[1,0,1]
	v_pk_add_f32 v[38:39], v[38:39], 1.0 op_sel_hi:[1,0]
	v_pk_add_f32 v[40:41], v[40:41], 1.0 op_sel_hi:[1,0]
	v_rcp_f32_e32 v38, v38
	v_rcp_f32_e32 v39, v39
	v_rcp_f32_e32 v40, v40
	v_rcp_f32_e32 v41, v41
	v_med3_f32 v42, v42, s2, v250
	v_med3_f32 v43, v43, s2, v250
	v_med3_f32 v44, v44, s2, v250
	v_med3_f32 v45, v45, s2, v250
	v_pk_mul_f32 v[34:35], v[34:35], v[38:39]
	v_pk_mul_f32 v[36:37], v[36:37], v[40:41]
	v_pk_mul_f32 v[48:49], v[42:43], v[34:35]
	v_pk_mul_f32 v[50:51], v[44:45], v[36:37]
	v_pk_fma_f32 v[34:35], v[104:105], s[100:101], v[4:5] op_sel_hi:[1,0,1]
	v_pk_fma_f32 v[36:37], v[106:107], s[100:101], v[6:7] op_sel_hi:[1,0,1]
	v_min_f32_e32 v34, 0x40e00000, v34
	v_min_f32_e32 v35, 0x40e00000, v35
	v_min_f32_e32 v36, 0x40e00000, v36
	v_min_f32_e32 v37, 0x40e00000, v37
	v_pk_mul_f32 v[38:39], v[34:35], s[100:101] op_sel:[0,1] op_sel_hi:[1,1]
	v_pk_mul_f32 v[40:41], v[36:37], s[100:101] op_sel:[0,1] op_sel_hi:[1,1]
	v_exp_f32_e32 v38, v38
	v_exp_f32_e32 v39, v39
	v_exp_f32_e32 v40, v40
	v_exp_f32_e32 v41, v41
	v_pk_fma_f32 v[42:43], v[12:13], s[100:101], v[22:23] op_sel_hi:[1,0,1]
	v_pk_fma_f32 v[44:45], v[14:15], s[100:101], v[20:21] op_sel_hi:[1,0,1]
	v_pk_add_f32 v[38:39], v[38:39], 1.0 op_sel_hi:[1,0]
	v_pk_add_f32 v[40:41], v[40:41], 1.0 op_sel_hi:[1,0]
	v_rcp_f32_e32 v38, v38
	v_rcp_f32_e32 v39, v39
	v_rcp_f32_e32 v40, v40
	v_rcp_f32_e32 v41, v41
	v_med3_f32 v42, v42, s2, v250
	v_med3_f32 v43, v43, s2, v250
	v_med3_f32 v44, v44, s2, v250
	v_med3_f32 v45, v45, s2, v250
	v_pk_mul_f32 v[34:35], v[34:35], v[38:39]
	v_pk_mul_f32 v[36:37], v[36:37], v[40:41]
	v_pk_mul_f32 v[52:53], v[42:43], v[34:35]
	v_pk_mul_f32 v[54:55], v[44:45], v[36:37]
	v_cvt_pk_fp8_f32 v58, v48, v49
	v_cvt_pk_fp8_f32 v58, v50, v51 op_sel:[0,0,1]
	v_cvt_pk_fp8_f32 v59, v52, v53
	v_cvt_pk_fp8_f32 v59, v54, v55 op_sel:[0,0,1]
	global_store_dwordx2 v[56:57], v[58:59], off sc1
